# v042 + S5 carry folded into the tail of the conv|F phase on workgroups 0-63 (F published write-through + counter hand-off); carry phase body and its seam skipped
# speedup vs baseline: 1.0043x; 1.0043x over previous
; #define PG8_STAGE(bufoff, gbase, voff) do { _Pragma("unroll") for (int _i = 0; _i < 2; ++_i) \
;         __builtin_amdgcn_global_load_lds((const unsigned*)((const char*)(gbase) + (voff)[_i]), (LAS unsigned*)(lds + (bufoff) + ldsw + _i * 8192), 16, 0, 0); } while (0)
; #define PG8_STAGE_A(bufoff, gbase, h, isnext) do { if constexpr (GATHER) { if (isnext) PG8_STAGE(bufoff, gbase, gAn[h]); else PG8_STAGE(bufoff, gbase, gA[h]); } \
;         else PG8_STAGE(bufoff, (gbase) + ((h) ? hstepA : (size_t)0), voffA); } while (0)
; #define PG8_GIDX(dst, u) do { _Pragma("unroll") for (int h_ = 0; h_ < 2; ++h_) _Pragma("unroll") for (int i_ = 0; i_ < 2; ++i_) { int R_, C_; stage_rc(tid * 16 + i_ * 8192, R_, C_); \
;         dst[h_][i_] = (unsigned)(*(const GAS int*)(g.gidx + (u).pm * 256 + h_ * 128 + R_)) * (unsigned)g.lda + (unsigned)(C_ * 2); } } while (0)
; #define PG8_WAIT_V(n) asm volatile("s_waitcnt vmcnt(" #n ")" ::: "memory")
; #define PG8_BAR __builtin_amdgcn_s_barrier()
; template <class Epi, class Sched, bool ALIGN_EPI, bool FP8 = false, bool GATHER = false>
; __device__ __forceinline__ void gemm_phase(LAS unsigned char* lds, const int tid, const Dims g, const Sched& S, const Epi& E) {
;     ...
;     const char* cA = cur.a; const char* cB = cur.b;
;     unsigned gA[2][2], gAn[2][2];
;     if constexpr (GATHER) { PG8_GIDX(gA, cur); _Pragma("unroll") for (int h_ = 0; h_ < 2; ++h_) _Pragma("unroll") for (int i_ = 0; i_ < 2; ++i_) gAn[h_][i_] = gA[h_][i_]; }
;     PG8_STAGE(PG8_SB(0, 0), cB, voffB); PG8_STAGE(PG8_SB(0, 1), cB + hstepB, voffB); PG8_STAGE_A(PG8_SA(0, 0), cA, 0, false); PG8_STAGE_A(PG8_SA(0, 1), cA, 1, false);
;     if (wr == 1) PG8_BAR;
;     PG8_WAIT_V(2); PG8_BAR;
;     PG8_STAGE(PG8_SB(1, 0), cB + kstep, voffB); PG8_STAGE_A(PG8_SA(1, 0), cA + kstep, 0, false); PG8_STAGE(PG8_SB(1, 1), cB + hstepB + kstep, voffB);
;     PG8_WAIT_V(6); PG8_BAR;
;     for (;;) {
;         const bool has_next = S.next(ui + 1, nxt);
;         const char* nA = has_next ? nxt.a : cA; const char* nB = has_next ? nxt.b : cB;
;         if constexpr (PG8_PEEL) { PG8_TRIP(0, false, PG8_MMAZ);
.LBB0_423:
	s_lshl_b32 s5, s5, 5
	s_add_i32 s29, 0, 0x18000
	s_and_b32 s15, s5, 0x60
	s_add_i32 s16, s29, s28
	s_mov_b64 s[6:7], 0x80
	s_lshl_b32 s26, s4, 13
	s_lshl_b32 s5, s15, 7
	v_lshl_add_u64 v[134:135], v[158:159], 0, s[6:7]
	s_mov_b32 m0, s16
	s_add_i32 s18, s16, 0x2000
	s_add_i32 s17, s24, 0x8000
	s_add_i32 s19, s24, 0xa000
	s_waitcnt vmcnt(2)
	s_barrier
	global_load_lds_dwordx4 v[134:135], off
	v_lshl_add_u64 v[136:137], v[160:161], 0, s[6:7]
	s_mov_b32 m0, s18
	v_lshl_add_u64 v[132:133], v[152:153], 0, s[6:7]
	v_lshl_add_u64 v[138:139], v[154:155], 0, s[6:7]
	s_add_u32 s6, s10, 0x20080
	global_load_lds_dwordx4 v[136:137], off
	s_mov_b32 m0, s17
	s_addc_u32 s7, s11, 0
	s_add_i32 s30, 0, 0x1c000
	global_load_lds_dwordx4 v[132:133], off
	s_mov_b32 m0, s19
	s_add_i32 s20, s30, s28
	global_load_lds_dwordx4 v[138:139], off
	v_lshl_add_u64 v[140:141], s[6:7], 0, v[130:131]
	s_mov_b32 m0, s20
	s_add_i32 s21, s20, 0x2000
	global_load_lds_dwordx4 v[140:141], off
	v_lshl_add_u64 v[142:143], s[6:7], 0, v[164:165]
	s_mov_b32 m0, s21
	v_and_b32_e32 v2, 15, v0
	global_load_lds_dwordx4 v[142:143], off
	v_and_b32_e32 v1, 48, v0
	v_lshlrev_b32_e32 v4, 2, v0
	v_lshl_or_b32 v3, v2, 6, v1
	v_and_b32_e32 v4, 32, v4
	v_bitop3_b32 v210, s5, v3, v4 bitop3:0xf6
	s_add_i32 s31, 0, 0x10000
	s_add_i32 s41, 0, 0x14000
	v_add_u32_e32 v168, s31, v210
	v_add_u32_e32 v169, s41, v210
	s_waitcnt vmcnt(6)
	s_barrier
	ds_read_b128 v[6:9], v168
	ds_read_b128 v[10:13], v168 offset:1024
	ds_read_b128 v[22:25], v168 offset:2048
	ds_read_b128 v[26:29], v168 offset:3072
	ds_read_b128 v[170:173], v169
	ds_read_b128 v[174:177], v169 offset:1024
	ds_read_b128 v[178:181], v169 offset:2048
	ds_read_b128 v[182:185], v169 offset:3072
	v_lshl_or_b32 v166, s4, 6, v2
	v_bitop3_b32 v2, v3, s26, v4 bitop3:0xde
	s_mov_b32 s4, 0
	s_add_u32 s6, s8, 0x28080
	s_addc_u32 s7, s9, 0
	s_add_i32 s27, s24, 0xc000
	v_add_u32_e32 v167, 0, v2
	v_lshl_add_u64 v[2:3], s[6:7], 0, v[162:163]
	s_mov_b32 m0, s27
	s_add_i32 s26, s24, 0xe000
	ds_read_b128 v[14:17], v167
	ds_read_b128 v[18:21], v167 offset:1024
	ds_read_b128 v[46:49], v167 offset:2048
	ds_read_b128 v[50:53], v167 offset:3072
	ds_read_b128 v[54:57], v167 offset:4096
	ds_read_b128 v[58:61], v167 offset:5120
	ds_read_b128 v[82:85], v167 offset:6144
	ds_read_b128 v[86:89], v167 offset:7168
	global_load_lds_dwordx4 v[2:3], off
	v_lshl_add_u64 v[2:3], s[6:7], 0, v[148:149]
	s_mov_b32 m0, s26
	s_nop 0
	global_load_lds_dwordx4 v[2:3], off
	s_waitcnt vmcnt(8)
	s_waitcnt lgkmcnt(0)
	s_barrier
	s_setprio 1
	s_mov_b32 s6, s4
	s_mov_b32 s7, s4
	s_mov_b32 s5, s4
	v_mov_b64_e32 v[124:125], s[6:7]
	v_mov_b64_e32 v[116:117], s[6:7]
	v_mov_b64_e32 v[108:109], s[6:7]
	v_mov_b64_e32 v[100:101], s[6:7]
	v_mov_b64_e32 v[76:77], s[6:7]
	v_mov_b64_e32 v[68:69], s[6:7]
	v_mov_b64_e32 v[44:45], s[6:7]
	v_mov_b64_e32 v[36:37], s[6:7]
	v_mov_b64_e32 v[2:3], s[4:5]
	v_mov_b64_e32 v[122:123], s[4:5]
	v_mov_b64_e32 v[114:115], s[4:5]
	v_mov_b64_e32 v[106:107], s[4:5]
	v_mov_b64_e32 v[98:99], s[4:5]
	v_mov_b64_e32 v[74:75], s[4:5]
	v_mov_b64_e32 v[66:67], s[4:5]
	v_mov_b64_e32 v[42:43], s[4:5]
	v_mov_b64_e32 v[34:35], s[4:5]
	v_mov_b64_e32 v[4:5], s[6:7]
	s_waitcnt lgkmcnt(0)
	v_mfma_f32_16x16x128_f8f6f4 v[122:125], v[6:13], v[14:21], 0
	v_mfma_f32_16x16x128_f8f6f4 v[114:117], v[22:29], v[14:21], 0
	v_mfma_f32_16x16x128_f8f6f4 v[106:109], v[6:13], v[46:53], 0
	v_mfma_f32_16x16x128_f8f6f4 v[98:101], v[22:29], v[46:53], 0
	v_mfma_f32_16x16x128_f8f6f4 v[74:77], v[6:13], v[54:61], 0
	v_mfma_f32_16x16x128_f8f6f4 v[66:69], v[22:29], v[54:61], 0
	v_mfma_f32_16x16x128_f8f6f4 v[42:45], v[6:13], v[82:89], 0
	v_mfma_f32_16x16x128_f8f6f4 v[34:37], v[22:29], v[82:89], 0
	s_setprio 0
	s_setprio 1
	v_mov_b64_e32 v[128:129], s[6:7]
	v_mov_b64_e32 v[120:121], s[6:7]
	v_mov_b64_e32 v[112:113], s[6:7]
	v_mov_b64_e32 v[104:105], s[6:7]
	v_mov_b64_e32 v[126:127], s[4:5]
	v_mov_b64_e32 v[118:119], s[4:5]
	v_mov_b64_e32 v[110:111], s[4:5]
	v_mov_b64_e32 v[102:103], s[4:5]
	v_mfma_f32_16x16x128_f8f6f4 v[126:129], v[170:177], v[14:21], 0
	v_mfma_f32_16x16x128_f8f6f4 v[118:121], v[178:185], v[14:21], 0
	v_mfma_f32_16x16x128_f8f6f4 v[110:113], v[170:177], v[46:53], 0
	v_mfma_f32_16x16x128_f8f6f4 v[102:105], v[178:185], v[46:53], 0
	v_mov_b64_e32 v[80:81], s[6:7]
	v_mov_b64_e32 v[72:73], s[6:7]
	v_mov_b64_e32 v[48:49], s[6:7]
	v_mov_b64_e32 v[40:41], s[6:7]
	v_mov_b64_e32 v[78:79], s[4:5]
	v_mov_b64_e32 v[70:71], s[4:5]
	v_mov_b64_e32 v[46:47], s[4:5]
	v_mov_b64_e32 v[38:39], s[4:5]
	v_mfma_f32_16x16x128_f8f6f4 v[78:81], v[170:177], v[54:61], 0
	v_mfma_f32_16x16x128_f8f6f4 v[70:73], v[178:185], v[54:61], 0
	v_mfma_f32_16x16x128_f8f6f4 v[46:49], v[170:177], v[82:89], 0
	v_mfma_f32_16x16x128_f8f6f4 v[38:41], v[178:185], v[82:89], 0
	s_setprio 0
	s_barrier
	s_add_i32 s4, s31, s28
	s_mov_b64 s[34:35], 0x100
	s_add_i32 s5, s4, 0x2000
	v_lshl_add_u64 v[14:15], v[158:159], 0, s[34:35]
	s_mov_b32 m0, s4
	s_add_u32 s36, s10, 0x20100
	ds_read_b128 v[54:57], v167 offset:16384
	ds_read_b128 v[58:61], v167 offset:17408
	ds_read_b128 v[186:189], v167 offset:18432
	ds_read_b128 v[190:193], v167 offset:19456
	ds_read_b128 v[194:197], v167 offset:20480
	ds_read_b128 v[198:201], v167 offset:21504
	ds_read_b128 v[202:205], v167 offset:22528
	ds_read_b128 v[206:209], v167 offset:23552
	global_load_lds_dwordx4 v[14:15], off
	v_lshl_add_u64 v[14:15], v[160:161], 0, s[34:35]
	s_mov_b32 m0, s5
	s_addc_u32 s37, s11, 0
	s_add_i32 s6, s41, s28
	global_load_lds_dwordx4 v[14:15], off
	v_lshl_add_u64 v[14:15], s[36:37], 0, v[130:131]
	s_mov_b32 m0, s6
	s_add_i32 s7, s6, 0x2000
	global_load_lds_dwordx4 v[14:15], off
	v_lshl_add_u64 v[14:15], s[36:37], 0, v[164:165]
	s_mov_b32 m0, s7
	s_nop 0
	global_load_lds_dwordx4 v[14:15], off
	v_lshl_add_u64 v[14:15], v[152:153], 0, s[34:35]
	s_mov_b32 m0, s24
	s_nop 0
	global_load_lds_dwordx4 v[14:15], off
	v_lshl_add_u64 v[14:15], v[154:155], 0, s[34:35]
	s_mov_b32 m0, s25
	s_nop 0
	global_load_lds_dwordx4 v[14:15], off
	s_waitcnt vmcnt(8)
	s_waitcnt lgkmcnt(0)
	s_barrier
	s_setprio 1
	v_mov_b64_e32 v[96:97], v[4:5]
	v_mov_b64_e32 v[84:85], v[4:5]
	v_mov_b64_e32 v[64:65], v[4:5]
	v_mov_b64_e32 v[52:53], v[4:5]
	v_mov_b64_e32 v[32:33], v[4:5]
	v_mov_b64_e32 v[20:21], v[4:5]
	v_mov_b64_e32 v[16:17], v[4:5]
	v_mov_b64_e32 v[94:95], v[2:3]
	v_mov_b64_e32 v[82:83], v[2:3]
	v_mov_b64_e32 v[62:63], v[2:3]
	v_mov_b64_e32 v[50:51], v[2:3]
	v_mov_b64_e32 v[30:31], v[2:3]
	v_mov_b64_e32 v[18:19], v[2:3]
	v_mov_b64_e32 v[14:15], v[2:3]
	s_waitcnt lgkmcnt(0)
	v_mfma_f32_16x16x128_f8f6f4 v[94:97], v[6:13], v[54:61], 0
	v_mfma_f32_16x16x128_f8f6f4 v[82:85], v[22:29], v[54:61], 0
	v_mfma_f32_16x16x128_f8f6f4 v[62:65], v[6:13], v[186:193], 0
	v_mfma_f32_16x16x128_f8f6f4 v[50:53], v[22:29], v[186:193], 0
	v_mfma_f32_16x16x128_f8f6f4 v[30:33], v[6:13], v[194:201], 0
	v_mfma_f32_16x16x128_f8f6f4 v[18:21], v[22:29], v[194:201], 0
	v_mfma_f32_16x16x128_f8f6f4 v[14:17], v[6:13], v[202:209], 0
	v_mov_b64_e32 v[8:9], v[4:5]
	v_mov_b64_e32 v[6:7], v[2:3]
	v_mfma_f32_16x16x128_f8f6f4 v[6:9], v[22:29], v[202:209], 0
	s_setprio 0
	s_setprio 1
	v_mov_b64_e32 v[92:93], v[4:5]
	v_mov_b64_e32 v[88:89], v[4:5]
	v_mov_b64_e32 v[90:91], v[2:3]
	v_mov_b64_e32 v[86:87], v[2:3]
	v_mfma_f32_16x16x128_f8f6f4 v[90:93], v[170:177], v[54:61], 0
	v_mfma_f32_16x16x128_f8f6f4 v[86:89], v[178:185], v[54:61], 0
	v_mov_b64_e32 v[60:61], v[4:5]
	v_mov_b64_e32 v[56:57], v[4:5]
	v_mov_b64_e32 v[28:29], v[4:5]
	v_mov_b64_e32 v[24:25], v[4:5]
	v_mov_b64_e32 v[12:13], v[4:5]
	v_mov_b64_e32 v[58:59], v[2:3]
	v_mov_b64_e32 v[54:55], v[2:3]
	v_mov_b64_e32 v[26:27], v[2:3]
	v_mov_b64_e32 v[22:23], v[2:3]
	v_mov_b64_e32 v[10:11], v[2:3]
	v_mfma_f32_16x16x128_f8f6f4 v[58:61], v[170:177], v[186:193], 0
	v_mfma_f32_16x16x128_f8f6f4 v[54:57], v[178:185], v[186:193], 0
	v_mfma_f32_16x16x128_f8f6f4 v[26:29], v[170:177], v[194:201], 0
	v_mfma_f32_16x16x128_f8f6f4 v[22:25], v[178:185], v[194:201], 0
	v_mfma_f32_16x16x128_f8f6f4 v[10:13], v[170:177], v[202:209], 0
	v_mfma_f32_16x16x128_f8f6f4 v[2:5], v[178:185], v[202:209], 0
	s_setprio 0
	s_barrier
	v_add_u32_e32 v170, s29, v210
	v_add_u32_e32 v171, s30, v210
	ds_read_b128 v[172:175], v170
	ds_read_b128 v[176:179], v170 offset:1024
	ds_read_b128 v[180:183], v170 offset:2048
	ds_read_b128 v[184:187], v170 offset:3072
	ds_read_b128 v[188:191], v171
	ds_read_b128 v[192:195], v171 offset:1024
	ds_read_b128 v[196:199], v171 offset:2048
	ds_read_b128 v[200:203], v171 offset:3072
	s_add_u32 s28, s8, 0x28100
	s_addc_u32 s29, s9, 0
	s_mov_b32 m0, s22
	v_lshl_add_u64 v[236:237], s[28:29], 0, v[162:163]
	ds_read_b128 v[204:207], v167 offset:32768
	ds_read_b128 v[208:211], v167 offset:33792
	ds_read_b128 v[212:215], v167 offset:34816
	ds_read_b128 v[216:219], v167 offset:35840
	ds_read_b128 v[220:223], v167 offset:36864
	ds_read_b128 v[224:227], v167 offset:37888
	ds_read_b128 v[228:231], v167 offset:38912
	ds_read_b128 v[232:235], v167 offset:39936
	global_load_lds_dwordx4 v[236:237], off
	v_lshl_add_u64 v[236:237], s[28:29], 0, v[148:149]
	s_mov_b32 m0, s23
	s_nop 0
	global_load_lds_dwordx4 v[236:237], off
	s_waitcnt vmcnt(8)
	s_waitcnt lgkmcnt(0)
	s_barrier
	s_setprio 1
	s_waitcnt lgkmcnt(0)
	v_mfma_f32_16x16x128_f8f6f4 v[122:125], v[172:179], v[204:211], v[122:125]
	v_mfma_f32_16x16x128_f8f6f4 v[114:117], v[180:187], v[204:211], v[114:117]
	v_mfma_f32_16x16x128_f8f6f4 v[106:109], v[172:179], v[212:219], v[106:109]
	v_mfma_f32_16x16x128_f8f6f4 v[98:101], v[180:187], v[212:219], v[98:101]
	v_mfma_f32_16x16x128_f8f6f4 v[74:77], v[172:179], v[220:227], v[74:77]
	v_mfma_f32_16x16x128_f8f6f4 v[66:69], v[180:187], v[220:227], v[66:69]
	v_mfma_f32_16x16x128_f8f6f4 v[42:45], v[172:179], v[228:235], v[42:45]
	v_mfma_f32_16x16x128_f8f6f4 v[34:37], v[180:187], v[228:235], v[34:37]
	s_setprio 0
	s_setprio 1
	v_mfma_f32_16x16x128_f8f6f4 v[126:129], v[188:195], v[204:211], v[126:129]
	v_mfma_f32_16x16x128_f8f6f4 v[118:121], v[196:203], v[204:211], v[118:121]
	v_mfma_f32_16x16x128_f8f6f4 v[110:113], v[188:195], v[212:219], v[110:113]
	v_mfma_f32_16x16x128_f8f6f4 v[102:105], v[196:203], v[212:219], v[102:105]
	v_mfma_f32_16x16x128_f8f6f4 v[78:81], v[188:195], v[220:227], v[78:81]
	v_mfma_f32_16x16x128_f8f6f4 v[70:73], v[196:203], v[220:227], v[70:73]
	v_mfma_f32_16x16x128_f8f6f4 v[46:49], v[188:195], v[228:235], v[46:49]
	v_mfma_f32_16x16x128_f8f6f4 v[38:41], v[196:203], v[228:235], v[38:41]
	s_setprio 0
	s_barrier
	s_mov_b64 s[28:29], 0x180
	s_mov_b32 m0, s16
	v_lshl_add_u64 v[236:237], v[158:159], 0, s[28:29]
	s_add_u32 s30, s10, 0x20180
	ds_read_b128 v[204:207], v167 offset:49152
	ds_read_b128 v[208:211], v167 offset:50176
	ds_read_b128 v[212:215], v167 offset:51200
	ds_read_b128 v[216:219], v167 offset:52224
	ds_read_b128 v[220:223], v167 offset:53248
	ds_read_b128 v[224:227], v167 offset:54272
	ds_read_b128 v[228:231], v167 offset:55296
	ds_read_b128 v[232:235], v167 offset:56320
	global_load_lds_dwordx4 v[236:237], off
	v_lshl_add_u64 v[236:237], v[160:161], 0, s[28:29]
	s_mov_b32 m0, s18
	s_addc_u32 s31, s11, 0
	global_load_lds_dwordx4 v[236:237], off
	v_lshl_add_u64 v[236:237], s[30:31], 0, v[130:131]
	s_mov_b32 m0, s20
	s_nop 0
	global_load_lds_dwordx4 v[236:237], off
	v_lshl_add_u64 v[236:237], s[30:31], 0, v[164:165]
	s_mov_b32 m0, s21
	s_nop 0
	global_load_lds_dwordx4 v[236:237], off
	v_lshl_add_u64 v[236:237], v[152:153], 0, s[28:29]
	s_mov_b32 m0, s17
	s_nop 0
	global_load_lds_dwordx4 v[236:237], off
	v_lshl_add_u64 v[236:237], v[154:155], 0, s[28:29]
	s_mov_b32 m0, s19
	s_nop 0
	global_load_lds_dwordx4 v[236:237], off
	s_waitcnt vmcnt(8)
	s_waitcnt lgkmcnt(0)
	s_barrier
	s_setprio 1
	s_waitcnt lgkmcnt(0)
	v_mfma_f32_16x16x128_f8f6f4 v[94:97], v[172:179], v[204:211], v[94:97]
	v_mfma_f32_16x16x128_f8f6f4 v[82:85], v[180:187], v[204:211], v[82:85]
	v_mfma_f32_16x16x128_f8f6f4 v[62:65], v[172:179], v[212:219], v[62:65]
	v_mfma_f32_16x16x128_f8f6f4 v[50:53], v[180:187], v[212:219], v[50:53]
	v_mfma_f32_16x16x128_f8f6f4 v[30:33], v[172:179], v[220:227], v[30:33]
	v_mfma_f32_16x16x128_f8f6f4 v[18:21], v[180:187], v[220:227], v[18:21]
	v_mfma_f32_16x16x128_f8f6f4 v[14:17], v[172:179], v[228:235], v[14:17]
	v_mfma_f32_16x16x128_f8f6f4 v[6:9], v[180:187], v[228:235], v[6:9]
	s_setprio 0
	s_setprio 1
	v_mfma_f32_16x16x128_f8f6f4 v[90:93], v[188:195], v[204:211], v[90:93]
	v_mfma_f32_16x16x128_f8f6f4 v[86:89], v[196:203], v[204:211], v[86:89]
	v_mfma_f32_16x16x128_f8f6f4 v[58:61], v[188:195], v[212:219], v[58:61]
	v_mfma_f32_16x16x128_f8f6f4 v[54:57], v[196:203], v[212:219], v[54:57]
	v_mfma_f32_16x16x128_f8f6f4 v[26:29], v[188:195], v[220:227], v[26:29]
	v_mfma_f32_16x16x128_f8f6f4 v[22:25], v[196:203], v[220:227], v[22:25]
	v_mfma_f32_16x16x128_f8f6f4 v[10:13], v[188:195], v[228:235], v[10:13]
	v_mfma_f32_16x16x128_f8f6f4 v[2:5], v[196:203], v[228:235], v[2:5]
	s_setprio 0
	s_barrier
	ds_read_b128 v[172:175], v168
	ds_read_b128 v[176:179], v168 offset:1024
	ds_read_b128 v[180:183], v168 offset:2048
	ds_read_b128 v[184:187], v168 offset:3072
	ds_read_b128 v[188:191], v169
	ds_read_b128 v[192:195], v169 offset:1024
	ds_read_b128 v[196:199], v169 offset:2048
	ds_read_b128 v[200:203], v169 offset:3072
	s_add_u32 s28, s8, 0x28180
	s_addc_u32 s29, s9, 0
	s_mov_b32 m0, s27
	v_lshl_add_u64 v[236:237], s[28:29], 0, v[162:163]
	ds_read_b128 v[204:207], v167
	ds_read_b128 v[208:211], v167 offset:1024
	ds_read_b128 v[212:215], v167 offset:2048
	ds_read_b128 v[216:219], v167 offset:3072
	ds_read_b128 v[220:223], v167 offset:4096
	ds_read_b128 v[224:227], v167 offset:5120
	ds_read_b128 v[228:231], v167 offset:6144
	ds_read_b128 v[232:235], v167 offset:7168
	global_load_lds_dwordx4 v[236:237], off
	v_lshl_add_u64 v[236:237], s[28:29], 0, v[148:149]
	s_mov_b32 m0, s26
	s_nop 0
	global_load_lds_dwordx4 v[236:237], off
	s_waitcnt vmcnt(8)
	s_waitcnt lgkmcnt(0)
	s_barrier
	s_setprio 1
	s_waitcnt lgkmcnt(0)
	v_mfma_f32_16x16x128_f8f6f4 v[122:125], v[172:179], v[204:211], v[122:125]
	v_mfma_f32_16x16x128_f8f6f4 v[114:117], v[180:187], v[204:211], v[114:117]
	v_mfma_f32_16x16x128_f8f6f4 v[106:109], v[172:179], v[212:219], v[106:109]
	v_mfma_f32_16x16x128_f8f6f4 v[98:101], v[180:187], v[212:219], v[98:101]
	v_mfma_f32_16x16x128_f8f6f4 v[74:77], v[172:179], v[220:227], v[74:77]
	v_mfma_f32_16x16x128_f8f6f4 v[66:69], v[180:187], v[220:227], v[66:69]
	v_mfma_f32_16x16x128_f8f6f4 v[42:45], v[172:179], v[228:235], v[42:45]
	v_mfma_f32_16x16x128_f8f6f4 v[34:37], v[180:187], v[228:235], v[34:37]
	s_setprio 0
	s_setprio 1
	v_mfma_f32_16x16x128_f8f6f4 v[126:129], v[188:195], v[204:211], v[126:129]
	v_mfma_f32_16x16x128_f8f6f4 v[118:121], v[196:203], v[204:211], v[118:121]
	v_mfma_f32_16x16x128_f8f6f4 v[110:113], v[188:195], v[212:219], v[110:113]
	v_mfma_f32_16x16x128_f8f6f4 v[102:105], v[196:203], v[212:219], v[102:105]
	v_mfma_f32_16x16x128_f8f6f4 v[78:81], v[188:195], v[220:227], v[78:81]
	v_mfma_f32_16x16x128_f8f6f4 v[70:73], v[196:203], v[220:227], v[70:73]
	v_mfma_f32_16x16x128_f8f6f4 v[46:49], v[188:195], v[228:235], v[46:49]
	v_mfma_f32_16x16x128_f8f6f4 v[38:41], v[196:203], v[228:235], v[38:41]
	s_setprio 0
	s_barrier
	s_mov_b64 s[28:29], 0x200
	s_mov_b32 m0, s4
	v_lshl_add_u64 v[236:237], v[158:159], 0, s[28:29]
	s_add_u32 s30, s10, 0x20200
	ds_read_b128 v[204:207], v167 offset:16384
	ds_read_b128 v[208:211], v167 offset:17408
	ds_read_b128 v[212:215], v167 offset:18432
	ds_read_b128 v[216:219], v167 offset:19456
	ds_read_b128 v[220:223], v167 offset:20480
	ds_read_b128 v[224:227], v167 offset:21504
	ds_read_b128 v[228:231], v167 offset:22528
	ds_read_b128 v[232:235], v167 offset:23552
	global_load_lds_dwordx4 v[236:237], off
	v_lshl_add_u64 v[236:237], v[160:161], 0, s[28:29]
	s_mov_b32 m0, s5
	s_addc_u32 s31, s11, 0
	global_load_lds_dwordx4 v[236:237], off
	v_lshl_add_u64 v[236:237], s[30:31], 0, v[130:131]
	s_mov_b32 m0, s6
	s_nop 0
	global_load_lds_dwordx4 v[236:237], off
	v_lshl_add_u64 v[236:237], s[30:31], 0, v[164:165]
	s_mov_b32 m0, s7
	s_nop 0
	global_load_lds_dwordx4 v[236:237], off
	v_lshl_add_u64 v[236:237], v[152:153], 0, s[28:29]
	s_mov_b32 m0, s24
	s_nop 0
	global_load_lds_dwordx4 v[236:237], off
	v_lshl_add_u64 v[236:237], v[154:155], 0, s[28:29]
	s_mov_b32 m0, s25
	s_nop 0
	global_load_lds_dwordx4 v[236:237], off
	s_waitcnt vmcnt(8)
	s_waitcnt lgkmcnt(0)
	s_barrier
	s_setprio 1
	s_waitcnt lgkmcnt(0)
	v_mfma_f32_16x16x128_f8f6f4 v[94:97], v[172:179], v[204:211], v[94:97]
	v_mfma_f32_16x16x128_f8f6f4 v[82:85], v[180:187], v[204:211], v[82:85]
	v_mfma_f32_16x16x128_f8f6f4 v[62:65], v[172:179], v[212:219], v[62:65]
	v_mfma_f32_16x16x128_f8f6f4 v[50:53], v[180:187], v[212:219], v[50:53]
	v_mfma_f32_16x16x128_f8f6f4 v[30:33], v[172:179], v[220:227], v[30:33]
	v_mfma_f32_16x16x128_f8f6f4 v[18:21], v[180:187], v[220:227], v[18:21]
	v_mfma_f32_16x16x128_f8f6f4 v[14:17], v[172:179], v[228:235], v[14:17]
	v_mfma_f32_16x16x128_f8f6f4 v[6:9], v[180:187], v[228:235], v[6:9]
	s_setprio 0
	s_setprio 1
	v_mfma_f32_16x16x128_f8f6f4 v[90:93], v[188:195], v[204:211], v[90:93]
	v_mfma_f32_16x16x128_f8f6f4 v[86:89], v[196:203], v[204:211], v[86:89]
	v_mfma_f32_16x16x128_f8f6f4 v[58:61], v[188:195], v[212:219], v[58:61]
	v_mfma_f32_16x16x128_f8f6f4 v[54:57], v[196:203], v[212:219], v[54:57]
	v_mfma_f32_16x16x128_f8f6f4 v[26:29], v[188:195], v[220:227], v[26:29]
	v_mfma_f32_16x16x128_f8f6f4 v[22:25], v[196:203], v[220:227], v[22:25]
	v_mfma_f32_16x16x128_f8f6f4 v[10:13], v[188:195], v[228:235], v[10:13]
	v_mfma_f32_16x16x128_f8f6f4 v[2:5], v[196:203], v[228:235], v[2:5]
	s_setprio 0
	s_barrier
	ds_read_b128 v[172:175], v170
	ds_read_b128 v[176:179], v170 offset:1024
	ds_read_b128 v[180:183], v170 offset:2048
	ds_read_b128 v[184:187], v170 offset:3072
	ds_read_b128 v[188:191], v171
	ds_read_b128 v[192:195], v171 offset:1024
	ds_read_b128 v[196:199], v171 offset:2048
	ds_read_b128 v[200:203], v171 offset:3072
	s_add_u32 s28, s8, 0x28200
	s_addc_u32 s29, s9, 0
	s_mov_b32 m0, s22
	v_lshl_add_u64 v[236:237], s[28:29], 0, v[162:163]
	ds_read_b128 v[204:207], v167 offset:32768
	ds_read_b128 v[208:211], v167 offset:33792
	ds_read_b128 v[212:215], v167 offset:34816
	ds_read_b128 v[216:219], v167 offset:35840
	ds_read_b128 v[220:223], v167 offset:36864
	ds_read_b128 v[224:227], v167 offset:37888
	ds_read_b128 v[228:231], v167 offset:38912
	ds_read_b128 v[232:235], v167 offset:39936
	global_load_lds_dwordx4 v[236:237], off
	v_lshl_add_u64 v[236:237], s[28:29], 0, v[148:149]
	s_mov_b32 m0, s23
	s_nop 0
	global_load_lds_dwordx4 v[236:237], off
	s_waitcnt vmcnt(8)
	s_waitcnt lgkmcnt(0)
	s_barrier
	s_setprio 1
	s_waitcnt lgkmcnt(0)
	v_mfma_f32_16x16x128_f8f6f4 v[122:125], v[172:179], v[204:211], v[122:125]
	v_mfma_f32_16x16x128_f8f6f4 v[114:117], v[180:187], v[204:211], v[114:117]
	v_mfma_f32_16x16x128_f8f6f4 v[106:109], v[172:179], v[212:219], v[106:109]
	v_mfma_f32_16x16x128_f8f6f4 v[98:101], v[180:187], v[212:219], v[98:101]
	v_mfma_f32_16x16x128_f8f6f4 v[74:77], v[172:179], v[220:227], v[74:77]
	v_mfma_f32_16x16x128_f8f6f4 v[66:69], v[180:187], v[220:227], v[66:69]
	v_mfma_f32_16x16x128_f8f6f4 v[42:45], v[172:179], v[228:235], v[42:45]
	v_mfma_f32_16x16x128_f8f6f4 v[34:37], v[180:187], v[228:235], v[34:37]
	s_setprio 0
	s_setprio 1
	v_mfma_f32_16x16x128_f8f6f4 v[126:129], v[188:195], v[204:211], v[126:129]
	v_mfma_f32_16x16x128_f8f6f4 v[118:121], v[196:203], v[204:211], v[118:121]
	v_mfma_f32_16x16x128_f8f6f4 v[110:113], v[188:195], v[212:219], v[110:113]
	v_mfma_f32_16x16x128_f8f6f4 v[102:105], v[196:203], v[212:219], v[102:105]
	v_mfma_f32_16x16x128_f8f6f4 v[78:81], v[188:195], v[220:227], v[78:81]
	v_mfma_f32_16x16x128_f8f6f4 v[70:73], v[196:203], v[220:227], v[70:73]
	v_mfma_f32_16x16x128_f8f6f4 v[46:49], v[188:195], v[228:235], v[46:49]
	v_mfma_f32_16x16x128_f8f6f4 v[38:41], v[196:203], v[228:235], v[38:41]
	s_setprio 0
	s_barrier
	s_mov_b64 s[28:29], 0x280
	s_mov_b32 m0, s16
	v_lshl_add_u64 v[236:237], v[158:159], 0, s[28:29]
	s_add_u32 s30, s10, 0x20280
	ds_read_b128 v[204:207], v167 offset:49152
	ds_read_b128 v[208:211], v167 offset:50176
	ds_read_b128 v[212:215], v167 offset:51200
	ds_read_b128 v[216:219], v167 offset:52224
	ds_read_b128 v[220:223], v167 offset:53248
	ds_read_b128 v[224:227], v167 offset:54272
	ds_read_b128 v[228:231], v167 offset:55296
	ds_read_b128 v[232:235], v167 offset:56320
	global_load_lds_dwordx4 v[236:237], off
	v_lshl_add_u64 v[236:237], v[160:161], 0, s[28:29]
	s_mov_b32 m0, s18
	s_addc_u32 s31, s11, 0
	global_load_lds_dwordx4 v[236:237], off
	v_lshl_add_u64 v[236:237], s[30:31], 0, v[130:131]
	s_mov_b32 m0, s20
	s_nop 0
	global_load_lds_dwordx4 v[236:237], off
	v_lshl_add_u64 v[236:237], s[30:31], 0, v[164:165]
	s_mov_b32 m0, s21
	s_nop 0
	global_load_lds_dwordx4 v[236:237], off
	v_lshl_add_u64 v[236:237], v[152:153], 0, s[28:29]
	s_mov_b32 m0, s17
	s_nop 0
	global_load_lds_dwordx4 v[236:237], off
	v_lshl_add_u64 v[236:237], v[154:155], 0, s[28:29]
	s_mov_b32 m0, s19
	s_nop 0
	global_load_lds_dwordx4 v[236:237], off
	s_waitcnt vmcnt(8)
	s_waitcnt lgkmcnt(0)
	s_barrier
	s_setprio 1
	s_waitcnt lgkmcnt(0)
	v_mfma_f32_16x16x128_f8f6f4 v[94:97], v[172:179], v[204:211], v[94:97]
	v_mfma_f32_16x16x128_f8f6f4 v[82:85], v[180:187], v[204:211], v[82:85]
	v_mfma_f32_16x16x128_f8f6f4 v[62:65], v[172:179], v[212:219], v[62:65]
	v_mfma_f32_16x16x128_f8f6f4 v[50:53], v[180:187], v[212:219], v[50:53]
	v_mfma_f32_16x16x128_f8f6f4 v[30:33], v[172:179], v[220:227], v[30:33]
	v_mfma_f32_16x16x128_f8f6f4 v[18:21], v[180:187], v[220:227], v[18:21]
	v_mfma_f32_16x16x128_f8f6f4 v[14:17], v[172:179], v[228:235], v[14:17]
	v_mfma_f32_16x16x128_f8f6f4 v[6:9], v[180:187], v[228:235], v[6:9]
	s_setprio 0
	s_setprio 1
	v_mfma_f32_16x16x128_f8f6f4 v[90:93], v[188:195], v[204:211], v[90:93]
	v_mfma_f32_16x16x128_f8f6f4 v[86:89], v[196:203], v[204:211], v[86:89]
	v_mfma_f32_16x16x128_f8f6f4 v[58:61], v[188:195], v[212:219], v[58:61]
	v_mfma_f32_16x16x128_f8f6f4 v[54:57], v[196:203], v[212:219], v[54:57]
	v_mfma_f32_16x16x128_f8f6f4 v[26:29], v[188:195], v[220:227], v[26:29]
	v_mfma_f32_16x16x128_f8f6f4 v[22:25], v[196:203], v[220:227], v[22:25]
	v_mfma_f32_16x16x128_f8f6f4 v[10:13], v[188:195], v[228:235], v[10:13]
	v_mfma_f32_16x16x128_f8f6f4 v[2:5], v[196:203], v[228:235], v[2:5]
	s_setprio 0
	s_barrier
	ds_read_b128 v[172:175], v168
	ds_read_b128 v[176:179], v168 offset:1024
	ds_read_b128 v[180:183], v168 offset:2048
	ds_read_b128 v[184:187], v168 offset:3072
	ds_read_b128 v[188:191], v169
	ds_read_b128 v[192:195], v169 offset:1024
	ds_read_b128 v[196:199], v169 offset:2048
	ds_read_b128 v[200:203], v169 offset:3072
	s_add_u32 s28, s8, 0x28280
	s_addc_u32 s29, s9, 0
	s_mov_b32 m0, s27
	v_lshl_add_u64 v[236:237], s[28:29], 0, v[162:163]
	ds_read_b128 v[204:207], v167
	ds_read_b128 v[208:211], v167 offset:1024
	ds_read_b128 v[212:215], v167 offset:2048
	ds_read_b128 v[216:219], v167 offset:3072
	ds_read_b128 v[220:223], v167 offset:4096
	ds_read_b128 v[224:227], v167 offset:5120
	ds_read_b128 v[228:231], v167 offset:6144
	ds_read_b128 v[232:235], v167 offset:7168
	global_load_lds_dwordx4 v[236:237], off
	v_lshl_add_u64 v[236:237], s[28:29], 0, v[148:149]
	s_mov_b32 m0, s26
	s_nop 0
	global_load_lds_dwordx4 v[236:237], off
	s_waitcnt vmcnt(8)
	s_waitcnt lgkmcnt(0)
	s_barrier
	s_setprio 1
	s_waitcnt lgkmcnt(0)
	v_mfma_f32_16x16x128_f8f6f4 v[122:125], v[172:179], v[204:211], v[122:125]
	v_mfma_f32_16x16x128_f8f6f4 v[114:117], v[180:187], v[204:211], v[114:117]
	v_mfma_f32_16x16x128_f8f6f4 v[106:109], v[172:179], v[212:219], v[106:109]
	v_mfma_f32_16x16x128_f8f6f4 v[98:101], v[180:187], v[212:219], v[98:101]
	v_mfma_f32_16x16x128_f8f6f4 v[74:77], v[172:179], v[220:227], v[74:77]
	v_mfma_f32_16x16x128_f8f6f4 v[66:69], v[180:187], v[220:227], v[66:69]
	v_mfma_f32_16x16x128_f8f6f4 v[42:45], v[172:179], v[228:235], v[42:45]
	v_mfma_f32_16x16x128_f8f6f4 v[34:37], v[180:187], v[228:235], v[34:37]
	s_setprio 0
	s_setprio 1
	v_mfma_f32_16x16x128_f8f6f4 v[126:129], v[188:195], v[204:211], v[126:129]
	v_mfma_f32_16x16x128_f8f6f4 v[118:121], v[196:203], v[204:211], v[118:121]
	v_mfma_f32_16x16x128_f8f6f4 v[110:113], v[188:195], v[212:219], v[110:113]
	v_mfma_f32_16x16x128_f8f6f4 v[102:105], v[196:203], v[212:219], v[102:105]
	v_mfma_f32_16x16x128_f8f6f4 v[78:81], v[188:195], v[220:227], v[78:81]
	v_mfma_f32_16x16x128_f8f6f4 v[70:73], v[196:203], v[220:227], v[70:73]
	v_mfma_f32_16x16x128_f8f6f4 v[46:49], v[188:195], v[228:235], v[46:49]
	v_mfma_f32_16x16x128_f8f6f4 v[38:41], v[196:203], v[228:235], v[38:41]
	s_setprio 0
	s_barrier
	s_mov_b64 s[28:29], 0x300
	s_mov_b32 m0, s4
	v_lshl_add_u64 v[236:237], v[158:159], 0, s[28:29]
	s_add_u32 s30, s10, 0x20300
	ds_read_b128 v[204:207], v167 offset:16384
	ds_read_b128 v[208:211], v167 offset:17408
	ds_read_b128 v[212:215], v167 offset:18432
	ds_read_b128 v[216:219], v167 offset:19456
	ds_read_b128 v[220:223], v167 offset:20480
	ds_read_b128 v[224:227], v167 offset:21504
	ds_read_b128 v[228:231], v167 offset:22528
	ds_read_b128 v[232:235], v167 offset:23552
	global_load_lds_dwordx4 v[236:237], off
	v_lshl_add_u64 v[236:237], v[160:161], 0, s[28:29]
	s_mov_b32 m0, s5
	s_addc_u32 s31, s11, 0
	global_load_lds_dwordx4 v[236:237], off
	v_lshl_add_u64 v[236:237], s[30:31], 0, v[130:131]
	s_mov_b32 m0, s6
	s_nop 0
	global_load_lds_dwordx4 v[236:237], off
	v_lshl_add_u64 v[236:237], s[30:31], 0, v[164:165]
	s_mov_b32 m0, s7
	s_nop 0
	global_load_lds_dwordx4 v[236:237], off
	v_lshl_add_u64 v[236:237], v[152:153], 0, s[28:29]
	s_mov_b32 m0, s24
	s_nop 0
	global_load_lds_dwordx4 v[236:237], off
	v_lshl_add_u64 v[236:237], v[154:155], 0, s[28:29]
	s_mov_b32 m0, s25
	s_nop 0
	global_load_lds_dwordx4 v[236:237], off
	s_waitcnt vmcnt(8)
	s_waitcnt lgkmcnt(0)
	s_barrier
	s_setprio 1
	s_waitcnt lgkmcnt(0)
	v_mfma_f32_16x16x128_f8f6f4 v[94:97], v[172:179], v[204:211], v[94:97]
	v_mfma_f32_16x16x128_f8f6f4 v[82:85], v[180:187], v[204:211], v[82:85]
	v_mfma_f32_16x16x128_f8f6f4 v[62:65], v[172:179], v[212:219], v[62:65]
	v_mfma_f32_16x16x128_f8f6f4 v[50:53], v[180:187], v[212:219], v[50:53]
	v_mfma_f32_16x16x128_f8f6f4 v[30:33], v[172:179], v[220:227], v[30:33]
	v_mfma_f32_16x16x128_f8f6f4 v[18:21], v[180:187], v[220:227], v[18:21]
	v_mfma_f32_16x16x128_f8f6f4 v[14:17], v[172:179], v[228:235], v[14:17]
	v_mfma_f32_16x16x128_f8f6f4 v[6:9], v[180:187], v[228:235], v[6:9]
	s_setprio 0
	s_setprio 1
	v_mfma_f32_16x16x128_f8f6f4 v[90:93], v[188:195], v[204:211], v[90:93]
	v_mfma_f32_16x16x128_f8f6f4 v[86:89], v[196:203], v[204:211], v[86:89]
	v_mfma_f32_16x16x128_f8f6f4 v[58:61], v[188:195], v[212:219], v[58:61]
	v_mfma_f32_16x16x128_f8f6f4 v[54:57], v[196:203], v[212:219], v[54:57]
	v_mfma_f32_16x16x128_f8f6f4 v[26:29], v[188:195], v[220:227], v[26:29]
	v_mfma_f32_16x16x128_f8f6f4 v[22:25], v[196:203], v[220:227], v[22:25]
	v_mfma_f32_16x16x128_f8f6f4 v[10:13], v[188:195], v[228:235], v[10:13]
	v_mfma_f32_16x16x128_f8f6f4 v[2:5], v[196:203], v[228:235], v[2:5]
	s_setprio 0
	s_barrier
	ds_read_b128 v[172:175], v170
	ds_read_b128 v[176:179], v170 offset:1024
	ds_read_b128 v[180:183], v170 offset:2048
	ds_read_b128 v[184:187], v170 offset:3072
	ds_read_b128 v[188:191], v171
	ds_read_b128 v[192:195], v171 offset:1024
	ds_read_b128 v[196:199], v171 offset:2048
	ds_read_b128 v[200:203], v171 offset:3072
	s_add_u32 s28, s8, 0x28300
	s_addc_u32 s29, s9, 0
	s_mov_b32 m0, s22
	v_lshl_add_u64 v[236:237], s[28:29], 0, v[162:163]
	ds_read_b128 v[204:207], v167 offset:32768
	ds_read_b128 v[208:211], v167 offset:33792
	ds_read_b128 v[212:215], v167 offset:34816
	ds_read_b128 v[216:219], v167 offset:35840
	ds_read_b128 v[220:223], v167 offset:36864
	ds_read_b128 v[224:227], v167 offset:37888
	ds_read_b128 v[228:231], v167 offset:38912
	ds_read_b128 v[232:235], v167 offset:39936
	global_load_lds_dwordx4 v[236:237], off
	v_lshl_add_u64 v[236:237], s[28:29], 0, v[148:149]
	s_mov_b32 m0, s23
	s_nop 0
	global_load_lds_dwordx4 v[236:237], off
	s_waitcnt vmcnt(8)
	s_waitcnt lgkmcnt(0)
	s_barrier
	s_setprio 1
	s_waitcnt lgkmcnt(0)
	v_mfma_f32_16x16x128_f8f6f4 v[122:125], v[172:179], v[204:211], v[122:125]
	v_mfma_f32_16x16x128_f8f6f4 v[114:117], v[180:187], v[204:211], v[114:117]
	v_mfma_f32_16x16x128_f8f6f4 v[106:109], v[172:179], v[212:219], v[106:109]
	v_mfma_f32_16x16x128_f8f6f4 v[98:101], v[180:187], v[212:219], v[98:101]
	v_mfma_f32_16x16x128_f8f6f4 v[74:77], v[172:179], v[220:227], v[74:77]
	v_mfma_f32_16x16x128_f8f6f4 v[66:69], v[180:187], v[220:227], v[66:69]
	v_mfma_f32_16x16x128_f8f6f4 v[42:45], v[172:179], v[228:235], v[42:45]
	v_mfma_f32_16x16x128_f8f6f4 v[34:37], v[180:187], v[228:235], v[34:37]
	s_setprio 0
	s_setprio 1
	v_mfma_f32_16x16x128_f8f6f4 v[126:129], v[188:195], v[204:211], v[126:129]
	v_mfma_f32_16x16x128_f8f6f4 v[118:121], v[196:203], v[204:211], v[118:121]
	v_mfma_f32_16x16x128_f8f6f4 v[110:113], v[188:195], v[212:219], v[110:113]
	v_mfma_f32_16x16x128_f8f6f4 v[102:105], v[196:203], v[212:219], v[102:105]
	v_mfma_f32_16x16x128_f8f6f4 v[78:81], v[188:195], v[220:227], v[78:81]
	v_mfma_f32_16x16x128_f8f6f4 v[70:73], v[196:203], v[220:227], v[70:73]
	v_mfma_f32_16x16x128_f8f6f4 v[46:49], v[188:195], v[228:235], v[46:49]
	v_mfma_f32_16x16x128_f8f6f4 v[38:41], v[196:203], v[228:235], v[38:41]
	s_setprio 0
	s_barrier
	s_mov_b64 s[28:29], 0x380
	s_mov_b32 m0, s16
	v_lshl_add_u64 v[236:237], v[158:159], 0, s[28:29]
	s_add_u32 s10, s10, 0x20380
	ds_read_b128 v[204:207], v167 offset:49152
	ds_read_b128 v[208:211], v167 offset:50176
	ds_read_b128 v[212:215], v167 offset:51200
	ds_read_b128 v[216:219], v167 offset:52224
	ds_read_b128 v[220:223], v167 offset:53248
	ds_read_b128 v[224:227], v167 offset:54272
	ds_read_b128 v[228:231], v167 offset:55296
	ds_read_b128 v[232:235], v167 offset:56320
	global_load_lds_dwordx4 v[236:237], off
	v_lshl_add_u64 v[236:237], v[160:161], 0, s[28:29]
	s_mov_b32 m0, s18
	s_addc_u32 s11, s11, 0
	global_load_lds_dwordx4 v[236:237], off
	v_lshl_add_u64 v[236:237], s[10:11], 0, v[130:131]
	s_mov_b32 m0, s20
	v_lshl_add_u64 v[164:165], s[10:11], 0, v[164:165]
	global_load_lds_dwordx4 v[236:237], off
	s_mov_b32 m0, s21
	s_nop 0
	global_load_lds_dwordx4 v[164:165], off
	v_lshl_add_u64 v[164:165], v[152:153], 0, s[28:29]
	s_mov_b32 m0, s17
	s_nop 0
	global_load_lds_dwordx4 v[164:165], off
	v_lshl_add_u64 v[164:165], v[154:155], 0, s[28:29]
	s_mov_b32 m0, s19
	s_nop 0
	global_load_lds_dwordx4 v[164:165], off
	s_waitcnt vmcnt(8)
	s_waitcnt lgkmcnt(0)
	s_barrier
	s_setprio 1
	s_waitcnt lgkmcnt(0)
	v_mfma_f32_16x16x128_f8f6f4 v[94:97], v[172:179], v[204:211], v[94:97]
	v_mfma_f32_16x16x128_f8f6f4 v[82:85], v[180:187], v[204:211], v[82:85]
	v_mfma_f32_16x16x128_f8f6f4 v[62:65], v[172:179], v[212:219], v[62:65]
	v_mfma_f32_16x16x128_f8f6f4 v[50:53], v[180:187], v[212:219], v[50:53]
	v_mfma_f32_16x16x128_f8f6f4 v[30:33], v[172:179], v[220:227], v[30:33]
	v_mfma_f32_16x16x128_f8f6f4 v[18:21], v[180:187], v[220:227], v[18:21]
	v_mfma_f32_16x16x128_f8f6f4 v[14:17], v[172:179], v[228:235], v[14:17]
	v_mfma_f32_16x16x128_f8f6f4 v[6:9], v[180:187], v[228:235], v[6:9]
	s_setprio 0
	s_setprio 1
	v_mfma_f32_16x16x128_f8f6f4 v[90:93], v[188:195], v[204:211], v[90:93]
	v_mfma_f32_16x16x128_f8f6f4 v[86:89], v[196:203], v[204:211], v[86:89]
	v_mfma_f32_16x16x128_f8f6f4 v[58:61], v[188:195], v[212:219], v[58:61]
	v_mfma_f32_16x16x128_f8f6f4 v[54:57], v[196:203], v[212:219], v[54:57]
	v_mfma_f32_16x16x128_f8f6f4 v[26:29], v[188:195], v[220:227], v[26:29]
	v_mfma_f32_16x16x128_f8f6f4 v[22:25], v[196:203], v[220:227], v[22:25]
	v_mfma_f32_16x16x128_f8f6f4 v[10:13], v[188:195], v[228:235], v[10:13]
	v_mfma_f32_16x16x128_f8f6f4 v[2:5], v[196:203], v[228:235], v[2:5]
	s_setprio 0
	s_barrier
	ds_read_b128 v[172:175], v168
	ds_read_b128 v[176:179], v168 offset:1024
	ds_read_b128 v[180:183], v168 offset:2048
	ds_read_b128 v[184:187], v168 offset:3072
	ds_read_b128 v[188:191], v169
	ds_read_b128 v[192:195], v169 offset:1024
	ds_read_b128 v[196:199], v169 offset:2048
	ds_read_b128 v[200:203], v169 offset:3072
	s_add_u32 s8, s8, 0x28380
	s_addc_u32 s9, s9, 0
	s_mov_b32 m0, s27
	v_lshl_add_u64 v[162:163], s[8:9], 0, v[162:163]
	ds_read_b128 v[204:207], v167
	ds_read_b128 v[208:211], v167 offset:1024
	ds_read_b128 v[212:215], v167 offset:2048
	ds_read_b128 v[216:219], v167 offset:3072
	ds_read_b128 v[220:223], v167 offset:4096
	ds_read_b128 v[224:227], v167 offset:5120
	ds_read_b128 v[228:231], v167 offset:6144
	ds_read_b128 v[232:235], v167 offset:7168
	global_load_lds_dwordx4 v[162:163], off
	v_lshl_add_u64 v[148:149], s[8:9], 0, v[148:149]
	s_mov_b32 m0, s26
	s_nop 0
	global_load_lds_dwordx4 v[148:149], off
	s_waitcnt vmcnt(8)
	s_waitcnt lgkmcnt(0)
	s_barrier
	s_setprio 1
	s_waitcnt lgkmcnt(0)
	v_mfma_f32_16x16x128_f8f6f4 v[122:125], v[172:179], v[204:211], v[122:125]
	v_mfma_f32_16x16x128_f8f6f4 v[114:117], v[180:187], v[204:211], v[114:117]
	v_mfma_f32_16x16x128_f8f6f4 v[106:109], v[172:179], v[212:219], v[106:109]
	v_mfma_f32_16x16x128_f8f6f4 v[98:101], v[180:187], v[212:219], v[98:101]
	v_mfma_f32_16x16x128_f8f6f4 v[74:77], v[172:179], v[220:227], v[74:77]
	v_mfma_f32_16x16x128_f8f6f4 v[66:69], v[180:187], v[220:227], v[66:69]
	v_mfma_f32_16x16x128_f8f6f4 v[42:45], v[172:179], v[228:235], v[42:45]
	v_mfma_f32_16x16x128_f8f6f4 v[34:37], v[180:187], v[228:235], v[34:37]
	s_setprio 0
	s_setprio 1
	v_mfma_f32_16x16x128_f8f6f4 v[126:129], v[188:195], v[204:211], v[126:129]
	v_mfma_f32_16x16x128_f8f6f4 v[118:121], v[196:203], v[204:211], v[118:121]
	v_mfma_f32_16x16x128_f8f6f4 v[110:113], v[188:195], v[212:219], v[110:113]
	v_mfma_f32_16x16x128_f8f6f4 v[102:105], v[196:203], v[212:219], v[102:105]
	v_mfma_f32_16x16x128_f8f6f4 v[78:81], v[188:195], v[220:227], v[78:81]
	v_mfma_f32_16x16x128_f8f6f4 v[70:73], v[196:203], v[220:227], v[70:73]
	v_mfma_f32_16x16x128_f8f6f4 v[46:49], v[188:195], v[228:235], v[46:49]
	v_mfma_f32_16x16x128_f8f6f4 v[38:41], v[196:203], v[228:235], v[38:41]
	s_setprio 0
	s_barrier
	s_mov_b32 m0, s4
	ds_read_b128 v[204:207], v167 offset:16384
	ds_read_b128 v[208:211], v167 offset:17408
	ds_read_b128 v[212:215], v167 offset:18432
	ds_read_b128 v[216:219], v167 offset:19456
	ds_read_b128 v[220:223], v167 offset:20480
	ds_read_b128 v[224:227], v167 offset:21504
	ds_read_b128 v[228:231], v167 offset:22528
	ds_read_b128 v[232:235], v167 offset:23552
	global_load_lds_dwordx4 v[158:159], off
	s_mov_b32 m0, s5
	s_nop 0
	global_load_lds_dwordx4 v[160:161], off
	s_mov_b32 m0, s6
	s_nop 0
	global_load_lds_dwordx4 v[156:157], off
	s_mov_b32 m0, s7
	s_nop 0
	global_load_lds_dwordx4 v[150:151], off
	s_mov_b32 m0, s24
	s_nop 0
	global_load_lds_dwordx4 v[152:153], off
	s_mov_b32 m0, s25
	s_nop 0
	global_load_lds_dwordx4 v[154:155], off
	s_waitcnt vmcnt(8)
	s_waitcnt lgkmcnt(0)
	s_barrier
	s_setprio 1
	s_waitcnt lgkmcnt(0)
	v_mfma_f32_16x16x128_f8f6f4 v[94:97], v[172:179], v[204:211], v[94:97]
	v_mfma_f32_16x16x128_f8f6f4 v[82:85], v[180:187], v[204:211], v[82:85]
	v_mfma_f32_16x16x128_f8f6f4 v[62:65], v[172:179], v[212:219], v[62:65]
	v_mfma_f32_16x16x128_f8f6f4 v[50:53], v[180:187], v[212:219], v[50:53]
	v_mfma_f32_16x16x128_f8f6f4 v[30:33], v[172:179], v[220:227], v[30:33]
	v_mfma_f32_16x16x128_f8f6f4 v[18:21], v[180:187], v[220:227], v[18:21]
	v_mfma_f32_16x16x128_f8f6f4 v[14:17], v[172:179], v[228:235], v[14:17]
	v_mfma_f32_16x16x128_f8f6f4 v[6:9], v[180:187], v[228:235], v[6:9]
	s_setprio 0
	s_setprio 1
	v_mfma_f32_16x16x128_f8f6f4 v[90:93], v[188:195], v[204:211], v[90:93]
	v_mfma_f32_16x16x128_f8f6f4 v[86:89], v[196:203], v[204:211], v[86:89]
	v_mfma_f32_16x16x128_f8f6f4 v[58:61], v[188:195], v[212:219], v[58:61]
	v_mfma_f32_16x16x128_f8f6f4 v[54:57], v[196:203], v[212:219], v[54:57]
	v_mfma_f32_16x16x128_f8f6f4 v[26:29], v[188:195], v[220:227], v[26:29]
	v_mfma_f32_16x16x128_f8f6f4 v[22:25], v[196:203], v[220:227], v[22:25]
	v_mfma_f32_16x16x128_f8f6f4 v[10:13], v[188:195], v[228:235], v[10:13]
	v_mfma_f32_16x16x128_f8f6f4 v[2:5], v[196:203], v[228:235], v[2:5]
	s_setprio 0
	s_barrier
	ds_read_b128 v[148:151], v170
	ds_read_b128 v[152:155], v170 offset:1024
	ds_read_b128 v[156:159], v170 offset:2048
	ds_read_b128 v[160:163], v170 offset:3072
	ds_read_b128 v[172:175], v171
	ds_read_b128 v[176:179], v171 offset:1024
	ds_read_b128 v[180:183], v171 offset:2048
	ds_read_b128 v[184:187], v171 offset:3072
	s_mov_b32 m0, s22
	ds_read_b128 v[188:191], v167 offset:32768
	ds_read_b128 v[192:195], v167 offset:33792
	ds_read_b128 v[196:199], v167 offset:34816
	ds_read_b128 v[200:203], v167 offset:35840
	ds_read_b128 v[204:207], v167 offset:36864
	ds_read_b128 v[208:211], v167 offset:37888
	ds_read_b128 v[212:215], v167 offset:38912
	ds_read_b128 v[216:219], v167 offset:39936
	global_load_lds_dwordx4 v[144:145], off
	s_mov_b32 m0, s23
	s_nop 0
	global_load_lds_dwordx4 v[146:147], off
	s_waitcnt vmcnt(8)
	s_waitcnt lgkmcnt(0)
	s_barrier
	s_setprio 1
	s_waitcnt lgkmcnt(0)
	v_mfma_f32_16x16x128_f8f6f4 v[122:125], v[148:155], v[188:195], v[122:125]
	v_mfma_f32_16x16x128_f8f6f4 v[114:117], v[156:163], v[188:195], v[114:117]
	v_mfma_f32_16x16x128_f8f6f4 v[106:109], v[148:155], v[196:203], v[106:109]
	v_mfma_f32_16x16x128_f8f6f4 v[98:101], v[156:163], v[196:203], v[98:101]
	v_mfma_f32_16x16x128_f8f6f4 v[74:77], v[148:155], v[204:211], v[74:77]
	v_mfma_f32_16x16x128_f8f6f4 v[66:69], v[156:163], v[204:211], v[66:69]
	v_mfma_f32_16x16x128_f8f6f4 v[42:45], v[148:155], v[212:219], v[42:45]
	v_mfma_f32_16x16x128_f8f6f4 v[34:37], v[156:163], v[212:219], v[34:37]
	s_setprio 0
	s_setprio 1
	v_mfma_f32_16x16x128_f8f6f4 v[126:129], v[172:179], v[188:195], v[126:129]
	v_mfma_f32_16x16x128_f8f6f4 v[118:121], v[180:187], v[188:195], v[118:121]
	v_mfma_f32_16x16x128_f8f6f4 v[110:113], v[172:179], v[196:203], v[110:113]
	v_mfma_f32_16x16x128_f8f6f4 v[102:105], v[180:187], v[196:203], v[102:105]
	v_mfma_f32_16x16x128_f8f6f4 v[78:81], v[172:179], v[204:211], v[78:81]
	v_mfma_f32_16x16x128_f8f6f4 v[70:73], v[180:187], v[204:211], v[70:73]
	v_mfma_f32_16x16x128_f8f6f4 v[46:49], v[172:179], v[212:219], v[46:49]
	v_mfma_f32_16x16x128_f8f6f4 v[38:41], v[180:187], v[212:219], v[38:41]
	s_setprio 0
	s_barrier
	s_mov_b32 m0, s16
	ds_read_b128 v[188:191], v167 offset:49152
	ds_read_b128 v[192:195], v167 offset:50176
	ds_read_b128 v[196:199], v167 offset:51200
	ds_read_b128 v[200:203], v167 offset:52224
	ds_read_b128 v[204:207], v167 offset:53248
	ds_read_b128 v[208:211], v167 offset:54272
	ds_read_b128 v[212:215], v167 offset:55296
	ds_read_b128 v[216:219], v167 offset:56320
	global_load_lds_dwordx4 v[134:135], off
	s_mov_b32 m0, s18
	s_nop 0
	global_load_lds_dwordx4 v[136:137], off
	s_mov_b32 m0, s20
	s_nop 0
	global_load_lds_dwordx4 v[140:141], off
	s_mov_b32 m0, s21
	s_nop 0
	global_load_lds_dwordx4 v[142:143], off
	s_mov_b32 m0, s17
	s_nop 0
	global_load_lds_dwordx4 v[132:133], off
	s_mov_b32 m0, s19
	s_nop 0
	global_load_lds_dwordx4 v[138:139], off
	s_waitcnt vmcnt(8)
	s_waitcnt lgkmcnt(0)
	s_barrier
	s_setprio 1
	s_waitcnt lgkmcnt(0)
	v_mfma_f32_16x16x128_f8f6f4 v[94:97], v[148:155], v[188:195], v[94:97]
	v_mfma_f32_16x16x128_f8f6f4 v[82:85], v[156:163], v[188:195], v[82:85]
	v_mfma_f32_16x16x128_f8f6f4 v[62:65], v[148:155], v[196:203], v[62:65]
	v_mfma_f32_16x16x128_f8f6f4 v[50:53], v[156:163], v[196:203], v[50:53]
	v_mfma_f32_16x16x128_f8f6f4 v[30:33], v[148:155], v[204:211], v[30:33]
	v_mfma_f32_16x16x128_f8f6f4 v[18:21], v[156:163], v[204:211], v[18:21]
	v_mfma_f32_16x16x128_f8f6f4 v[14:17], v[148:155], v[212:219], v[14:17]
	v_mfma_f32_16x16x128_f8f6f4 v[6:9], v[156:163], v[212:219], v[6:9]
	s_setprio 0
	s_setprio 1
	v_mfma_f32_16x16x128_f8f6f4 v[90:93], v[172:179], v[188:195], v[90:93]
	v_mfma_f32_16x16x128_f8f6f4 v[86:89], v[180:187], v[188:195], v[86:89]
	v_mfma_f32_16x16x128_f8f6f4 v[58:61], v[172:179], v[196:203], v[58:61]
	v_mfma_f32_16x16x128_f8f6f4 v[54:57], v[180:187], v[196:203], v[54:57]
	v_mfma_f32_16x16x128_f8f6f4 v[26:29], v[172:179], v[204:211], v[26:29]
	v_mfma_f32_16x16x128_f8f6f4 v[22:25], v[180:187], v[204:211], v[22:25]
	v_mfma_f32_16x16x128_f8f6f4 v[10:13], v[172:179], v[212:219], v[10:13]
	v_mfma_f32_16x16x128_f8f6f4 v[2:5], v[180:187], v[212:219], v[2:5]
	s_setprio 0
	s_barrier
; #define GAS __attribute__((address_space(1)))
;     __device__ __forceinline__ void operator()(const f32x4 (&acc)[2][2][4][2], const Unit& u, int wr, int wc, int fr, int fq) const {
;         float* base = C + (size_t)u.aux * cstride; const int row0 = u.pm * 256 + wr * 64 + fr, col0 = u.pn * 256 + wc * 32 + 4 * fq;
; #pragma unroll
;         for (int ai = 0; ai < 2; ++ai)
; #pragma unroll
;             for (int m = 0; m < 4; ++m) { float* rowp = base + (size_t)(row0 + ai * 128 + m * 16) * ldc + col0;
; #pragma unroll
;                 for (int bj = 0; bj < 2; ++bj)
; #pragma unroll
;                     for (int n = 0; n < 2; ++n) *(GAS f32x4*)(rowp + bj * 128 + n * 16) = acc[ai][bj][m][n] * scale; }
	s_lshl_b64 s[2:3], s[2:3], 19
	s_add_u32 s2, s38, s2
	s_addc_u32 s3, s39, s3
	v_add_u32_e32 v132, s1, v166
	v_lshl_or_b32 v130, s15, 2, v1
	v_lshl_add_u64 v[130:131], s[2:3], 0, v[130:131]
	s_mov_b64 s[2:3], 0x56900000
	v_ashrrev_i32_e32 v133, 31, v132
	v_lshl_add_u64 v[134:135], v[130:131], 0, s[2:3]
	v_lshlrev_b64 v[130:131], 10, v[132:133]
	s_mov_b32 s2, 0x38800000
	v_lshl_add_u64 v[130:131], v[134:135], 0, v[130:131]
	v_pk_mul_f32 v[116:117], v[116:117], s[2:3] op_sel_hi:[1,0]
	v_pk_mul_f32 v[114:115], v[114:115], s[2:3] op_sel_hi:[1,0]
	s_nop 15
	s_nop 7
	global_store_dwordx4 v[130:131], v[114:117], off offset:64 sc1
	v_pk_mul_f32 v[100:101], v[100:101], s[2:3] op_sel_hi:[1,0]
	v_pk_mul_f32 v[98:99], v[98:99], s[2:3] op_sel_hi:[1,0]
	v_pk_mul_f32 v[116:117], v[128:129], s[2:3] op_sel_hi:[1,0]
	v_pk_mul_f32 v[114:115], v[126:127], s[2:3] op_sel_hi:[1,0]
	global_store_dwordx4 v[130:131], v[114:117], off offset:512 sc1
	v_pk_mul_f32 v[68:69], v[68:69], s[2:3] op_sel_hi:[1,0]
	v_pk_mul_f32 v[66:67], v[66:67], s[2:3] op_sel_hi:[1,0]
	v_pk_mul_f32 v[116:117], v[120:121], s[2:3] op_sel_hi:[1,0]
	v_pk_mul_f32 v[114:115], v[118:119], s[2:3] op_sel_hi:[1,0]
	global_store_dwordx4 v[130:131], v[114:117], off offset:576 sc1
	v_pk_mul_f32 v[36:37], v[36:37], s[2:3] op_sel_hi:[1,0]
	v_pk_mul_f32 v[34:35], v[34:35], s[2:3] op_sel_hi:[1,0]
	v_or_b32_e32 v114, 16, v132
	v_ashrrev_i32_e32 v115, 31, v114
	v_lshlrev_b64 v[114:115], 10, v[114:115]
	v_lshl_add_u64 v[114:115], v[134:135], 0, v[114:115]
	global_store_dwordx4 v[114:115], v[98:101], off offset:64 sc1
	s_mov_b32 s1, 0x20000
	s_mov_b64 s[4:5], 0x20000
	v_pk_mul_f32 v[100:101], v[112:113], s[2:3] op_sel_hi:[1,0]
	v_pk_mul_f32 v[98:99], v[110:111], s[2:3] op_sel_hi:[1,0]
	global_store_dwordx4 v[114:115], v[98:101], off offset:512 sc1
	v_pk_mul_f32 v[20:21], v[20:21], s[2:3] op_sel_hi:[1,0]
	v_pk_mul_f32 v[18:19], v[18:19], s[2:3] op_sel_hi:[1,0]
	v_pk_mul_f32 v[100:101], v[104:105], s[2:3] op_sel_hi:[1,0]
	v_pk_mul_f32 v[98:99], v[102:103], s[2:3] op_sel_hi:[1,0]
	global_store_dwordx4 v[114:115], v[98:101], off offset:576 sc1
	v_pk_mul_f32 v[8:9], v[8:9], s[2:3] op_sel_hi:[1,0]
	v_pk_mul_f32 v[6:7], v[6:7], s[2:3] op_sel_hi:[1,0]
	v_or_b32_e32 v98, 32, v132
	v_ashrrev_i32_e32 v99, 31, v98
	v_lshlrev_b64 v[98:99], 10, v[98:99]
	v_lshl_add_u64 v[98:99], v[134:135], 0, v[98:99]
	global_store_dwordx4 v[98:99], v[66:69], off offset:64 sc1
	v_pk_mul_f32 v[124:125], v[124:125], s[2:3] op_sel_hi:[1,0]
	v_pk_mul_f32 v[122:123], v[122:123], s[2:3] op_sel_hi:[1,0]
	v_pk_mul_f32 v[68:69], v[80:81], s[2:3] op_sel_hi:[1,0]
	v_pk_mul_f32 v[66:67], v[78:79], s[2:3] op_sel_hi:[1,0]
	global_store_dwordx4 v[98:99], v[66:69], off offset:512 sc1
	v_pk_mul_f32 v[108:109], v[108:109], s[2:3] op_sel_hi:[1,0]
	v_pk_mul_f32 v[106:107], v[106:107], s[2:3] op_sel_hi:[1,0]
	v_pk_mul_f32 v[68:69], v[72:73], s[2:3] op_sel_hi:[1,0]
	v_pk_mul_f32 v[66:67], v[70:71], s[2:3] op_sel_hi:[1,0]
	global_store_dwordx4 v[98:99], v[66:69], off offset:576 sc1
	v_pk_mul_f32 v[76:77], v[76:77], s[2:3] op_sel_hi:[1,0]
	v_pk_mul_f32 v[74:75], v[74:75], s[2:3] op_sel_hi:[1,0]
	v_or_b32_e32 v66, 48, v132
	v_ashrrev_i32_e32 v67, 31, v66
	v_lshlrev_b64 v[66:67], 10, v[66:67]
	v_lshl_add_u64 v[66:67], v[134:135], 0, v[66:67]
	global_store_dwordx4 v[66:67], v[34:37], off offset:64 sc1
	v_pk_mul_f32 v[44:45], v[44:45], s[2:3] op_sel_hi:[1,0]
	v_pk_mul_f32 v[42:43], v[42:43], s[2:3] op_sel_hi:[1,0]
	v_pk_mul_f32 v[36:37], v[48:49], s[2:3] op_sel_hi:[1,0]
	v_pk_mul_f32 v[34:35], v[46:47], s[2:3] op_sel_hi:[1,0]
	global_store_dwordx4 v[66:67], v[34:37], off offset:512 sc1
; #define GAS __attribute__((address_space(1)))
;     __device__ __forceinline__ void operator()(const f32x4 (&acc)[2][2][4][2], const Unit& u, int wr, int wc, int fr, int fq) const {
;         float* base = C + (size_t)u.aux * cstride; const int row0 = u.pm * 256 + wr * 64 + fr, col0 = u.pn * 256 + wc * 32 + 4 * fq;
; #pragma unroll
;         for (int ai = 0; ai < 2; ++ai)
; #pragma unroll
;             for (int m = 0; m < 4; ++m) { float* rowp = base + (size_t)(row0 + ai * 128 + m * 16) * ldc + col0;
; #pragma unroll
;                 for (int bj = 0; bj < 2; ++bj)
; #pragma unroll
;                     for (int n = 0; n < 2; ++n) *(GAS f32x4*)(rowp + bj * 128 + n * 16) = acc[ai][bj][m][n] * scale; }
	v_pk_mul_f32 v[32:33], v[32:33], s[2:3] op_sel_hi:[1,0]
	v_pk_mul_f32 v[30:31], v[30:31], s[2:3] op_sel_hi:[1,0]
	v_pk_mul_f32 v[36:37], v[40:41], s[2:3] op_sel_hi:[1,0]
	v_pk_mul_f32 v[34:35], v[38:39], s[2:3] op_sel_hi:[1,0]
	v_add_co_u32_e32 v40, vcc, s1, v130
	global_store_dwordx4 v[66:67], v[34:37], off offset:576 sc1
	s_nop 0
	v_addc_co_u32_e32 v41, vcc, 0, v131, vcc
	v_pk_mul_f32 v[36:37], v[96:97], s[2:3] op_sel_hi:[1,0]
	v_pk_mul_f32 v[34:35], v[94:95], s[2:3] op_sel_hi:[1,0]
	v_lshl_add_u64 v[38:39], v[130:131], 0, s[4:5]
	global_store_dwordx4 v[40:41], v[34:37], off sc1
	s_mov_b32 s1, 0x24000
	v_add_co_u32_e32 v40, vcc, s1, v130
	v_pk_mul_f32 v[36:37], v[84:85], s[2:3] op_sel_hi:[1,0]
	v_pk_mul_f32 v[34:35], v[82:83], s[2:3] op_sel_hi:[1,0]
	global_store_dwordx4 v[38:39], v[34:37], off offset:64 sc1
	s_mov_b64 s[4:5], 0x24000
	v_addc_co_u32_e32 v41, vcc, 0, v131, vcc
	v_pk_mul_f32 v[36:37], v[92:93], s[2:3] op_sel_hi:[1,0]
	v_pk_mul_f32 v[34:35], v[90:91], s[2:3] op_sel_hi:[1,0]
	global_store_dwordx4 v[38:39], v[34:37], off offset:512 sc1
	s_mov_b32 s1, 0x28000
	v_pk_mul_f32 v[16:17], v[16:17], s[2:3] op_sel_hi:[1,0]
	v_pk_mul_f32 v[36:37], v[88:89], s[2:3] op_sel_hi:[1,0]
	v_pk_mul_f32 v[34:35], v[86:87], s[2:3] op_sel_hi:[1,0]
	global_store_dwordx4 v[38:39], v[34:37], off offset:576 sc1
	v_lshl_add_u64 v[38:39], v[130:131], 0, s[4:5]
	s_mov_b64 s[4:5], 0x28000
	v_pk_mul_f32 v[36:37], v[64:65], s[2:3] op_sel_hi:[1,0]
	v_pk_mul_f32 v[34:35], v[62:63], s[2:3] op_sel_hi:[1,0]
	global_store_dwordx4 v[40:41], v[34:37], off sc1
	v_pk_mul_f32 v[14:15], v[14:15], s[2:3] op_sel_hi:[1,0]
	v_pk_mul_f32 v[4:5], v[4:5], s[2:3] op_sel_hi:[1,0]
	v_pk_mul_f32 v[36:37], v[52:53], s[2:3] op_sel_hi:[1,0]
	v_pk_mul_f32 v[34:35], v[50:51], s[2:3] op_sel_hi:[1,0]
	global_store_dwordx4 v[38:39], v[34:37], off offset:64 sc1
	v_pk_mul_f32 v[2:3], v[2:3], s[2:3] op_sel_hi:[1,0]
	global_store_dwordx4 v[130:131], v[122:125], off sc1
	v_pk_mul_f32 v[36:37], v[60:61], s[2:3] op_sel_hi:[1,0]
	v_pk_mul_f32 v[34:35], v[58:59], s[2:3] op_sel_hi:[1,0]
	global_store_dwordx4 v[38:39], v[34:37], off offset:512 sc1
	global_store_dwordx4 v[114:115], v[106:109], off sc1
	global_store_dwordx4 v[98:99], v[74:77], off sc1
	v_pk_mul_f32 v[36:37], v[56:57], s[2:3] op_sel_hi:[1,0]
	v_pk_mul_f32 v[34:35], v[54:55], s[2:3] op_sel_hi:[1,0]
	global_store_dwordx4 v[38:39], v[34:37], off offset:576 sc1
	global_store_dwordx4 v[66:67], v[42:45], off sc1
	s_cmpk_gt_u32 s0, 0xff
	v_lshl_add_u64 v[34:35], v[130:131], 0, s[4:5]
	v_add_co_u32_e32 v36, vcc, s1, v130
	global_store_dwordx4 v[34:35], v[18:21], off offset:64 sc1
	s_nop 0
	v_addc_co_u32_e32 v37, vcc, 0, v131, vcc
	v_pk_mul_f32 v[20:21], v[28:29], s[2:3] op_sel_hi:[1,0]
	v_pk_mul_f32 v[18:19], v[26:27], s[2:3] op_sel_hi:[1,0]
	global_store_dwordx4 v[34:35], v[18:21], off offset:512 sc1
	s_mov_b64 s[4:5], 0x2c000
	s_mov_b32 s1, 0x2c000
	v_pk_mul_f32 v[20:21], v[24:25], s[2:3] op_sel_hi:[1,0]
	v_pk_mul_f32 v[18:19], v[22:23], s[2:3] op_sel_hi:[1,0]
	global_store_dwordx4 v[34:35], v[18:21], off offset:576 sc1
	global_store_dwordx4 v[36:37], v[30:33], off sc1
	s_nop 0
	v_lshl_add_u64 v[18:19], v[130:131], 0, s[4:5]
	v_add_co_u32_e32 v20, vcc, s1, v130
	global_store_dwordx4 v[18:19], v[6:9], off offset:64 sc1
	s_nop 0
	v_addc_co_u32_e32 v21, vcc, 0, v131, vcc
	v_pk_mul_f32 v[8:9], v[12:13], s[2:3] op_sel_hi:[1,0]
	v_pk_mul_f32 v[6:7], v[10:11], s[2:3] op_sel_hi:[1,0]
	global_store_dwordx4 v[20:21], v[14:17], off sc1
	global_store_dwordx4 v[18:19], v[6:9], off offset:512 sc1
	global_store_dwordx4 v[18:19], v[2:5], off offset:576 sc1
	s_waitcnt vmcnt(0)
	s_cbranch_scc1 .LBB0_425
	s_barrier

; #define PHASE(k) if constexpr (IN(k)) for (int rep_ = 0; rep_ < (((PROBE_MASK >> (k)) & 1u) ? 2 : 1); ++rep_)
; template <int LO, int HI, int l>
; __device__ __forceinline__ void layer_phases(Frame& F) {
;     ...
;     PHASE(pb + 2) {
;         launder(F);
;         if (F.vcu < F.G - 64) phase_conv(F, l, F.G - 64);
;         else { SchedF S{(const char*)WSP(unsigned char, WS_A8), (const char*)(WSP(unsigned char, WS_WF) + (size_t)l * NG * 256 * 1024), F.G, F.vcu};
;             EpiF32 E{WSP(float, WS_F), 256, (size_t)NINST * 256, S5_INV};
;             pg8::gemm_phase<EpiF32, SchedF, false, true>(F.lds, F.tid, pg8::Dims{KS2, 1024, 1024, nullptr}, S, E); }
;     }
.LBB0_426:
	s_waitcnt vmcnt(0) lgkmcnt(0)
	s_barrier
	v_cmp_eq_u32_e64 s[98:99], 0, v0
	s_and_saveexec_b64 s[100:101], s[98:99]
	s_cbranch_execz .Lfd0_pw
	v_mov_b32_e32 v2, s38
	v_mov_b32_e32 v3, s39
	v_mov_b32_e32 v4, 1
	flat_atomic_add v[2:3], v4 offset:3840
	s_waitcnt vmcnt(0) lgkmcnt(0)
.Lfd0_pw:
	s_or_b64 exec, exec, s[100:101]
	s_cbranch_execnz .LBB0_432
	s_branch .LBB0_429

; #define GAS __attribute__((address_space(1)))
; #define PHASE(k) if constexpr (IN(k)) for (int rep_ = 0; rep_ < (((PROBE_MASK >> (k)) & 1u) ? 2 : 1); ++rep_)
; __device__ __forceinline__ void phase_carry(Frame& F, int l) {
;     const int gt = F.vcu * 512 + F.tid; if (gt >= NB * NG * 2 * SP) return;
;     const int p = gt & 63, d = (gt >> 6) & 1, g = (gt >> 7) & 31, b = gt >> 12;
;     const f32x2 lt = WSP(f32x2, WS_LT)[((l * NG + g) * 2 + d) * 64 + p];
;     const float* Fb = WSP(float, WS_F); unsigned char* a8 = WSP(unsigned char, WS_A8);
;     float hr = 0.f, hi = 0.f;
;     float frv[36], fiv[36];
; #pragma unroll
;     for (int step = 0; step < 36; ++step) {
;         int inst; if (step < 4) inst = 256 + b * 4 + (d == 0 ? step : 3 - step); else inst = b * 32 + (d == 0 ? step - 4 : 35 - step);
;         const size_t row = (size_t)g * NINST + inst;
;         frv[step] = *(const GAS float*)(Fb + row * 256 + d * 128 + p); fiv[step] = *(const GAS float*)(Fb + row * 256 + d * 128 + 64 + p); }
; #pragma unroll
;     for (int step = 0; step < 36; ++step) {
;         int inst; if (step < 4) inst = 256 + b * 4 + (d == 0 ? step : 3 - step); else inst = b * 32 + (d == 0 ? step - 4 : 35 - step);
; template <int LO, int HI, int l>
; __device__ __forceinline__ void layer_phases(Frame& F) {
;     ...
;     PHASE(pb + 3) { launder(F); phase_carry(F, l); }
.LBB0_432:
	s_and_b32 s98, s95, 7
	s_lshl_b32 s98, s98, 5
	s_lshr_b32 s99, s95, 3
	s_add_i32 s98, s98, s99
	s_cmp_ge_u32 s98, 64
	s_cbranch_scc1 .Lfd0_done
	s_waitcnt vmcnt(0) lgkmcnt(0)
	v_cmp_eq_u32_e64 s[98:99], 0, v0
	s_and_saveexec_b64 s[100:101], s[98:99]
	s_cbranch_execz .Lfd0_w
	v_mov_b32_e32 v2, s38
	v_mov_b32_e32 v3, s39
	s_mov_b32 s98, 0
.Lfd0_poll:
	flat_load_dword v4, v[2:3] offset:3840 sc1
	s_waitcnt vmcnt(0) lgkmcnt(0)
	v_readfirstlane_b32 s99, v4
	s_add_u32 s98, s98, 1
	s_cmp_ge_u32 s99, 64
	s_cbranch_scc1 .Lfd0_go
	s_sleep 2
	s_cmp_lt_u32 s98, 0x4000
	s_cbranch_scc1 .Lfd0_poll
.Lfd0_go:
	buffer_inv sc1
	s_waitcnt vmcnt(0) lgkmcnt(0)
.Lfd0_w:
	s_or_b64 exec, exec, s[100:101]
	s_barrier
	v_writelane_b32 v254, s0, 0
	v_writelane_b32 v254, s1, 1
	v_writelane_b32 v254, s2, 2
	v_writelane_b32 v254, s3, 3
	v_writelane_b32 v254, s4, 4
	v_writelane_b32 v254, s5, 5
	v_writelane_b32 v254, s6, 6
	v_writelane_b32 v254, s7, 7
	v_writelane_b32 v254, s33, 8
	v_writelane_b32 v254, s38, 9
	v_mov_b32_e32 v1, s38
	v_mov_b32_e32 v2, s39
	s_nop 0
	s_nop 0
	v_readfirstlane_b32 s2, v1
	v_readfirstlane_b32 s3, v2
	v_mov_b32_e32 v1, s33
	v_mov_b32_e32 v2, s40
	s_nop 0
	v_readfirstlane_b32 s33, v1
	v_readfirstlane_b32 s38, v2
	v_mov_b32_e32 v1, s54
	v_mov_b32_e32 v2, s95
	s_nop 0
	v_readfirstlane_b32 s1, v1
	s_and_b32 s0, s1, 7
	s_cmp_eq_u32 s0, 0
	v_readfirstlane_b32 s0, v2
	s_cbranch_scc0 .Lfd0_479
	s_ashr_i32 s4, s0, 31
	s_lshr_b32 s4, s4, 29
	s_add_i32 s4, s0, s4
	s_ashr_i32 s5, s4, 3
	s_and_b32 s4, s4, -8
	s_ashr_i32 s1, s1, 3
	s_sub_i32 s0, s0, s4
	s_mul_i32 s0, s0, s1
	s_add_i32 s0, s0, s5

; #define GAS __attribute__((address_space(1)))
; __device__ __forceinline__ void phase_carry(Frame& F, int l) {
;     const int gt = F.vcu * 512 + F.tid; if (gt >= NB * NG * 2 * SP) return;
;     const int p = gt & 63, d = (gt >> 6) & 1, g = (gt >> 7) & 31, b = gt >> 12;
;     const f32x2 lt = WSP(f32x2, WS_LT)[((l * NG + g) * 2 + d) * 64 + p];
;     const float* Fb = WSP(float, WS_F); unsigned char* a8 = WSP(unsigned char, WS_A8);
;     float hr = 0.f, hi = 0.f;
;     float frv[36], fiv[36];
; #pragma unroll
;     for (int step = 0; step < 36; ++step) {
;         int inst; if (step < 4) inst = 256 + b * 4 + (d == 0 ? step : 3 - step); else inst = b * 32 + (d == 0 ? step - 4 : 35 - step);
;         const size_t row = (size_t)g * NINST + inst;
;         frv[step] = *(const GAS float*)(Fb + row * 256 + d * 128 + p); fiv[step] = *(const GAS float*)(Fb + row * 256 + d * 128 + 64 + p); }
; #pragma unroll
;     for (int step = 0; step < 36; ++step) {
;         int inst; if (step < 4) inst = 256 + b * 4 + (d == 0 ? step : 3 - step); else inst = b * 32 + (d == 0 ? step - 4 : 35 - step);
;         const size_t row = (size_t)g * NINST + inst;
;         a8[row * KS2 + 1024 + d * 128 + p] = (unsigned char)(pk4_fp8(hr * S5_SH, 0.f, 0.f, 0.f) & 0xffu); a8[row * KS2 + 1024 + d * 128 + 64 + p] = (unsigned char)(pk4_fp8(hi * S5_SH, 0.f, 0.f, 0.f) & 0xffu);
;         const float nr = lt.x * hr - lt.y * hi + frv[step]; hi = lt.x * hi + lt.y * hr + fiv[step]; hr = nr; }
; }
.Lfd0_481:
	s_or_b64 exec, exec, s[4:5]
	s_waitcnt vmcnt(0) lgkmcnt(0)
	v_readlane_b32 s0, v254, 0
	v_readlane_b32 s1, v254, 1
	v_readlane_b32 s2, v254, 2
	v_readlane_b32 s3, v254, 3
	v_readlane_b32 s4, v254, 4
	v_readlane_b32 s5, v254, 5
	v_readlane_b32 s6, v254, 6
	v_readlane_b32 s7, v254, 7
	v_readlane_b32 s33, v254, 8
	v_readlane_b32 s38, v254, 9

; #define PHASE(k) if constexpr (IN(k)) for (int rep_ = 0; rep_ < (((PROBE_MASK >> (k)) & 1u) ? 2 : 1); ++rep_)
; #define SEAM(k) do { if constexpr (IN(k) && IN((k) + 1)) grid_seam(F); } while (0)
; __device__ __forceinline__ void launder(Frame& F) { F.ws = opaque_ptr(F.ws); F.out = opaque_ptr(F.out);
;     int t = F.tid; asm volatile("" : "+v"(t)); F.tid = t; F.lane = t & 63; F.wave = __builtin_amdgcn_readfirstlane(t >> 6);
;     int g = gridDim.x, bx = blockIdx.x; asm volatile("" : "+v"(g), "+v"(bx)); g = __builtin_amdgcn_readfirstlane(g); bx = __builtin_amdgcn_readfirstlane(bx);
;     F.G = g; F.vcu = (g % 8 == 0) ? (bx % 8) * (g / 8) + bx / 8 : bx; }
; template <int LO, int HI, int l>
; __device__ __forceinline__ void layer_phases(Frame& F) {
;     ...
;     PHASE(pb + 3) { launder(F); phase_carry(F, l); }
;     SEAM(pb + 3);
.LBB0_477:
	s_or_b64 exec, exec, s[2:3]
	v_mov_b32_e32 v1, s38
	v_mov_b32_e32 v2, s39
	s_waitcnt lgkmcnt(0)
	s_barrier
	s_nop 0
	v_readfirstlane_b32 s2, v1
	v_readfirstlane_b32 s3, v2
	v_mov_b32_e32 v1, s33
	v_mov_b32_e32 v2, s40
	s_nop 0
	v_readfirstlane_b32 s33, v1
	v_readfirstlane_b32 s38, v2
	s_branch .Lfd0_end
	v_mov_b32_e32 v1, s54
	v_mov_b32_e32 v2, s95
	s_nop 0
	v_readfirstlane_b32 s1, v1
	s_and_b32 s0, s1, 7
	s_cmp_eq_u32 s0, 0
	v_readfirstlane_b32 s0, v2
	s_cbranch_scc0 .LBB0_479
	s_ashr_i32 s4, s0, 31
	s_lshr_b32 s4, s4, 29
	s_add_i32 s4, s0, s4
	s_ashr_i32 s5, s4, 3
	s_and_b32 s4, s4, -8
	s_ashr_i32 s1, s1, 3
	s_sub_i32 s0, s0, s4
	s_mul_i32 s0, s0, s1
	s_add_i32 s0, s0, s5

; #define PHASE(k) if constexpr (IN(k)) for (int rep_ = 0; rep_ < (((PROBE_MASK >> (k)) & 1u) ? 2 : 1); ++rep_)
; __device__ __forceinline__ void launder(Frame& F) { F.ws = opaque_ptr(F.ws); F.out = opaque_ptr(F.out);
;     int t = F.tid; asm volatile("" : "+v"(t)); F.tid = t; F.lane = t & 63; F.wave = __builtin_amdgcn_readfirstlane(t >> 6);
;     int g = gridDim.x, bx = blockIdx.x; asm volatile("" : "+v"(g), "+v"(bx)); g = __builtin_amdgcn_readfirstlane(g); bx = __builtin_amdgcn_readfirstlane(bx);
;     F.G = g; F.vcu = (g % 8 == 0) ? (bx % 8) * (g / 8) + bx / 8 : bx; }
; template <int LO, int HI, int l>
; __device__ __forceinline__ void layer_phases(Frame& F) {
;     ...
;     PHASE(pb + 4) {
;         launder(F);
;         SchedS2 S{(const char*)WSP(unsigned char, WS_A8), (const char*)(WSP(unsigned char, WS_W2) + (size_t)l * NG * 1024 * KS2), F.G, F.vcu, l};
;         EpiS2 E{WSP(bf16, WS_U2), F.in[I_SSMD] + (size_t)l * DSSM, WSP(bf16, WS_Z)};
;         pg8::gemm_phase<EpiS2, SchedS2, true, true>(F.lds, F.tid, pg8::Dims{KS2, KS2, KS2, nullptr}, S, E);
.Lfd0_end:
	v_mov_b32_e32 v1, s2
	v_mov_b32_e32 v2, s3
	s_waitcnt lgkmcnt(0)
	s_barrier
	s_nop 0
	v_readfirstlane_b32 s47, v1
	v_readfirstlane_b32 s48, v2
	v_mov_b32_e32 v1, s33
	v_mov_b32_e32 v2, s38
	s_nop 0
	v_readfirstlane_b32 s33, v1
	v_readfirstlane_b32 s46, v2
	v_mov_b32_e32 v1, s54
	v_mov_b32_e32 v2, s95
	s_nop 0
	v_readfirstlane_b32 s37, v1
	s_and_b32 s0, s37, 7
	s_cmp_eq_u32 s0, 0
	v_readfirstlane_b32 s49, v2
	s_cbranch_scc0 .LBB0_528
	s_ashr_i32 s1, s49, 31
	s_lshr_b32 s1, s1, 29
	s_add_i32 s1, s49, s1
	s_ashr_i32 s2, s1, 3
	s_and_b32 s1, s1, -8
	s_ashr_i32 s0, s37, 3
	s_sub_i32 s1, s49, s1
	s_mul_i32 s0, s1, s0
	s_add_i32 s49, s0, s2

; #define PG8_STAGE(bufoff, gbase, voff) do { _Pragma("unroll") for (int _i = 0; _i < 2; ++_i) \
;         __builtin_amdgcn_global_load_lds((const unsigned*)((const char*)(gbase) + (voff)[_i]), (LAS unsigned*)(lds + (bufoff) + ldsw + _i * 8192), 16, 0, 0); } while (0)
; #define PG8_STAGE_A(bufoff, gbase, h, isnext) do { if constexpr (GATHER) { if (isnext) PG8_STAGE(bufoff, gbase, gAn[h]); else PG8_STAGE(bufoff, gbase, gA[h]); } \
;         else PG8_STAGE(bufoff, (gbase) + ((h) ? hstepA : (size_t)0), voffA); } while (0)
; #define PG8_GIDX(dst, u) do { _Pragma("unroll") for (int h_ = 0; h_ < 2; ++h_) _Pragma("unroll") for (int i_ = 0; i_ < 2; ++i_) { int R_, C_; stage_rc(tid * 16 + i_ * 8192, R_, C_); \
;         dst[h_][i_] = (unsigned)(*(const GAS int*)(g.gidx + (u).pm * 256 + h_ * 128 + R_)) * (unsigned)g.lda + (unsigned)(C_ * 2); } } while (0)
; #define PG8_WAIT_V(n) asm volatile("s_waitcnt vmcnt(" #n ")" ::: "memory")
; #define PG8_BAR __builtin_amdgcn_s_barrier()
; template <class Epi, class Sched, bool ALIGN_EPI, bool FP8 = false, bool GATHER = false>
; __device__ __forceinline__ void gemm_phase(LAS unsigned char* lds, const int tid, const Dims g, const Sched& S, const Epi& E) {
;     ...
;     const char* cA = cur.a; const char* cB = cur.b;
;     unsigned gA[2][2], gAn[2][2];
;     if constexpr (GATHER) { PG8_GIDX(gA, cur); _Pragma("unroll") for (int h_ = 0; h_ < 2; ++h_) _Pragma("unroll") for (int i_ = 0; i_ < 2; ++i_) gAn[h_][i_] = gA[h_][i_]; }
;     PG8_STAGE(PG8_SB(0, 0), cB, voffB); PG8_STAGE(PG8_SB(0, 1), cB + hstepB, voffB); PG8_STAGE_A(PG8_SA(0, 0), cA, 0, false); PG8_STAGE_A(PG8_SA(0, 1), cA, 1, false);
;     if (wr == 1) PG8_BAR;
;     PG8_WAIT_V(2); PG8_BAR;
;     PG8_STAGE(PG8_SB(1, 0), cB + kstep, voffB); PG8_STAGE_A(PG8_SA(1, 0), cA + kstep, 0, false); PG8_STAGE(PG8_SB(1, 1), cB + hstepB + kstep, voffB);
;     PG8_WAIT_V(6); PG8_BAR;
;     for (;;) {
;         const bool has_next = S.next(ui + 1, nxt);
;         const char* nA = has_next ? nxt.a : cA; const char* nB = has_next ? nxt.b : cB;
;         if constexpr (PG8_PEEL) { PG8_TRIP(0, false, PG8_MMAZ);
.LBB0_1443:
	s_lshl_b32 s5, s5, 5
	s_add_i32 s29, 0, 0x18000
	s_and_b32 s15, s5, 0x60
	s_add_i32 s16, s29, s28
	s_mov_b64 s[6:7], 0x80
	s_lshl_b32 s26, s4, 13
	s_lshl_b32 s5, s15, 7
	v_lshl_add_u64 v[134:135], v[158:159], 0, s[6:7]
	s_mov_b32 m0, s16
	s_add_i32 s18, s16, 0x2000
	s_add_i32 s17, s24, 0x8000
	s_add_i32 s19, s24, 0xa000
	s_waitcnt vmcnt(2)
	s_barrier
	global_load_lds_dwordx4 v[134:135], off
	v_lshl_add_u64 v[136:137], v[160:161], 0, s[6:7]
	s_mov_b32 m0, s18
	v_lshl_add_u64 v[132:133], v[152:153], 0, s[6:7]
	v_lshl_add_u64 v[138:139], v[154:155], 0, s[6:7]
	s_add_u32 s6, s10, 0x20080
	global_load_lds_dwordx4 v[136:137], off
	s_mov_b32 m0, s17
	s_addc_u32 s7, s11, 0
	s_add_i32 s30, 0, 0x1c000
	global_load_lds_dwordx4 v[132:133], off
	s_mov_b32 m0, s19
	s_add_i32 s20, s30, s28
	global_load_lds_dwordx4 v[138:139], off
	v_lshl_add_u64 v[140:141], s[6:7], 0, v[130:131]
	s_mov_b32 m0, s20
	s_add_i32 s21, s20, 0x2000
	global_load_lds_dwordx4 v[140:141], off
	v_lshl_add_u64 v[142:143], s[6:7], 0, v[164:165]
	s_mov_b32 m0, s21
	v_and_b32_e32 v2, 15, v0
	global_load_lds_dwordx4 v[142:143], off
	v_and_b32_e32 v1, 48, v0
	v_lshlrev_b32_e32 v4, 2, v0
	v_lshl_or_b32 v3, v2, 6, v1
	v_and_b32_e32 v4, 32, v4
	v_bitop3_b32 v210, s5, v3, v4 bitop3:0xf6
	s_add_i32 s31, 0, 0x10000
	s_add_i32 s43, 0, 0x14000
	v_add_u32_e32 v168, s31, v210
	v_add_u32_e32 v169, s43, v210
	s_waitcnt vmcnt(6)
	s_barrier
	ds_read_b128 v[6:9], v168
	ds_read_b128 v[10:13], v168 offset:1024
	ds_read_b128 v[22:25], v168 offset:2048
	ds_read_b128 v[26:29], v168 offset:3072
	ds_read_b128 v[170:173], v169
	ds_read_b128 v[174:177], v169 offset:1024
	ds_read_b128 v[178:181], v169 offset:2048
	ds_read_b128 v[182:185], v169 offset:3072
	v_lshl_or_b32 v166, s4, 6, v2
	v_bitop3_b32 v2, v3, s26, v4 bitop3:0xde
	s_mov_b32 s4, 0
	s_add_u32 s6, s8, 0x28080
	s_addc_u32 s7, s9, 0
	s_add_i32 s27, s24, 0xc000
	v_add_u32_e32 v167, 0, v2
	v_lshl_add_u64 v[2:3], s[6:7], 0, v[162:163]
	s_mov_b32 m0, s27
	s_add_i32 s26, s24, 0xe000
	ds_read_b128 v[14:17], v167
	ds_read_b128 v[18:21], v167 offset:1024
	ds_read_b128 v[46:49], v167 offset:2048
	ds_read_b128 v[50:53], v167 offset:3072
	ds_read_b128 v[54:57], v167 offset:4096
	ds_read_b128 v[58:61], v167 offset:5120
	ds_read_b128 v[82:85], v167 offset:6144
	ds_read_b128 v[86:89], v167 offset:7168
	global_load_lds_dwordx4 v[2:3], off
	v_lshl_add_u64 v[2:3], s[6:7], 0, v[148:149]
	s_mov_b32 m0, s26
	s_nop 0
	global_load_lds_dwordx4 v[2:3], off
	s_waitcnt vmcnt(8)
	s_waitcnt lgkmcnt(0)
	s_barrier
	s_setprio 1
	s_mov_b32 s6, s4
	s_mov_b32 s7, s4
	s_mov_b32 s5, s4
	v_mov_b64_e32 v[124:125], s[6:7]
	v_mov_b64_e32 v[116:117], s[6:7]
	v_mov_b64_e32 v[108:109], s[6:7]
	v_mov_b64_e32 v[100:101], s[6:7]
	v_mov_b64_e32 v[76:77], s[6:7]
	v_mov_b64_e32 v[68:69], s[6:7]
	v_mov_b64_e32 v[44:45], s[6:7]
	v_mov_b64_e32 v[36:37], s[6:7]
	v_mov_b64_e32 v[2:3], s[4:5]
	v_mov_b64_e32 v[122:123], s[4:5]
	v_mov_b64_e32 v[114:115], s[4:5]
	v_mov_b64_e32 v[106:107], s[4:5]
	v_mov_b64_e32 v[98:99], s[4:5]
	v_mov_b64_e32 v[74:75], s[4:5]
	v_mov_b64_e32 v[66:67], s[4:5]
	v_mov_b64_e32 v[42:43], s[4:5]
	v_mov_b64_e32 v[34:35], s[4:5]
	v_mov_b64_e32 v[4:5], s[6:7]
	s_waitcnt lgkmcnt(0)
	v_mfma_f32_16x16x128_f8f6f4 v[122:125], v[6:13], v[14:21], 0
	v_mfma_f32_16x16x128_f8f6f4 v[114:117], v[22:29], v[14:21], 0
	v_mfma_f32_16x16x128_f8f6f4 v[106:109], v[6:13], v[46:53], 0
	v_mfma_f32_16x16x128_f8f6f4 v[98:101], v[22:29], v[46:53], 0
	v_mfma_f32_16x16x128_f8f6f4 v[74:77], v[6:13], v[54:61], 0
	v_mfma_f32_16x16x128_f8f6f4 v[66:69], v[22:29], v[54:61], 0
	v_mfma_f32_16x16x128_f8f6f4 v[42:45], v[6:13], v[82:89], 0
	v_mfma_f32_16x16x128_f8f6f4 v[34:37], v[22:29], v[82:89], 0
	s_setprio 0
	s_setprio 1
	v_mov_b64_e32 v[128:129], s[6:7]
	v_mov_b64_e32 v[120:121], s[6:7]
	v_mov_b64_e32 v[112:113], s[6:7]
	v_mov_b64_e32 v[104:105], s[6:7]
	v_mov_b64_e32 v[126:127], s[4:5]
	v_mov_b64_e32 v[118:119], s[4:5]
	v_mov_b64_e32 v[110:111], s[4:5]
	v_mov_b64_e32 v[102:103], s[4:5]
	v_mfma_f32_16x16x128_f8f6f4 v[126:129], v[170:177], v[14:21], 0
	v_mfma_f32_16x16x128_f8f6f4 v[118:121], v[178:185], v[14:21], 0
	v_mfma_f32_16x16x128_f8f6f4 v[110:113], v[170:177], v[46:53], 0
	v_mfma_f32_16x16x128_f8f6f4 v[102:105], v[178:185], v[46:53], 0
	v_mov_b64_e32 v[80:81], s[6:7]
	v_mov_b64_e32 v[72:73], s[6:7]
	v_mov_b64_e32 v[48:49], s[6:7]
	v_mov_b64_e32 v[40:41], s[6:7]
	v_mov_b64_e32 v[78:79], s[4:5]
	v_mov_b64_e32 v[70:71], s[4:5]
	v_mov_b64_e32 v[46:47], s[4:5]
	v_mov_b64_e32 v[38:39], s[4:5]
	v_mfma_f32_16x16x128_f8f6f4 v[78:81], v[170:177], v[54:61], 0
	v_mfma_f32_16x16x128_f8f6f4 v[70:73], v[178:185], v[54:61], 0
	v_mfma_f32_16x16x128_f8f6f4 v[46:49], v[170:177], v[82:89], 0
	v_mfma_f32_16x16x128_f8f6f4 v[38:41], v[178:185], v[82:89], 0
	s_setprio 0
	s_barrier
	s_add_i32 s4, s31, s28
	s_mov_b64 s[34:35], 0x100
	s_add_i32 s5, s4, 0x2000
	v_lshl_add_u64 v[14:15], v[158:159], 0, s[34:35]
	s_mov_b32 m0, s4
	s_add_u32 s36, s10, 0x20100
	ds_read_b128 v[54:57], v167 offset:16384
	ds_read_b128 v[58:61], v167 offset:17408
	ds_read_b128 v[186:189], v167 offset:18432
	ds_read_b128 v[190:193], v167 offset:19456
	ds_read_b128 v[194:197], v167 offset:20480
	ds_read_b128 v[198:201], v167 offset:21504
	ds_read_b128 v[202:205], v167 offset:22528
	ds_read_b128 v[206:209], v167 offset:23552
	global_load_lds_dwordx4 v[14:15], off
	v_lshl_add_u64 v[14:15], v[160:161], 0, s[34:35]
	s_mov_b32 m0, s5
	s_addc_u32 s37, s11, 0
	s_add_i32 s6, s43, s28
	global_load_lds_dwordx4 v[14:15], off
	v_lshl_add_u64 v[14:15], s[36:37], 0, v[130:131]
	s_mov_b32 m0, s6
	s_add_i32 s7, s6, 0x2000
	global_load_lds_dwordx4 v[14:15], off
	v_lshl_add_u64 v[14:15], s[36:37], 0, v[164:165]
	s_mov_b32 m0, s7
	s_nop 0
	global_load_lds_dwordx4 v[14:15], off
	v_lshl_add_u64 v[14:15], v[152:153], 0, s[34:35]
	s_mov_b32 m0, s24
	s_nop 0
	global_load_lds_dwordx4 v[14:15], off
	v_lshl_add_u64 v[14:15], v[154:155], 0, s[34:35]
	s_mov_b32 m0, s25
	s_nop 0
	global_load_lds_dwordx4 v[14:15], off
	s_waitcnt vmcnt(8)
	s_waitcnt lgkmcnt(0)
	s_barrier
	s_setprio 1
	v_mov_b64_e32 v[96:97], v[4:5]
	v_mov_b64_e32 v[84:85], v[4:5]
	v_mov_b64_e32 v[64:65], v[4:5]
	v_mov_b64_e32 v[52:53], v[4:5]
	v_mov_b64_e32 v[32:33], v[4:5]
	v_mov_b64_e32 v[20:21], v[4:5]
	v_mov_b64_e32 v[16:17], v[4:5]
	v_mov_b64_e32 v[94:95], v[2:3]
	v_mov_b64_e32 v[82:83], v[2:3]
	v_mov_b64_e32 v[62:63], v[2:3]
	v_mov_b64_e32 v[50:51], v[2:3]
	v_mov_b64_e32 v[30:31], v[2:3]
	v_mov_b64_e32 v[18:19], v[2:3]
	v_mov_b64_e32 v[14:15], v[2:3]
	s_waitcnt lgkmcnt(0)
	v_mfma_f32_16x16x128_f8f6f4 v[94:97], v[6:13], v[54:61], 0
	v_mfma_f32_16x16x128_f8f6f4 v[82:85], v[22:29], v[54:61], 0
	v_mfma_f32_16x16x128_f8f6f4 v[62:65], v[6:13], v[186:193], 0
	v_mfma_f32_16x16x128_f8f6f4 v[50:53], v[22:29], v[186:193], 0
	v_mfma_f32_16x16x128_f8f6f4 v[30:33], v[6:13], v[194:201], 0
	v_mfma_f32_16x16x128_f8f6f4 v[18:21], v[22:29], v[194:201], 0
	v_mfma_f32_16x16x128_f8f6f4 v[14:17], v[6:13], v[202:209], 0
	v_mov_b64_e32 v[8:9], v[4:5]
	v_mov_b64_e32 v[6:7], v[2:3]
	v_mfma_f32_16x16x128_f8f6f4 v[6:9], v[22:29], v[202:209], 0
	s_setprio 0
	s_setprio 1
	v_mov_b64_e32 v[92:93], v[4:5]
	v_mov_b64_e32 v[88:89], v[4:5]
	v_mov_b64_e32 v[90:91], v[2:3]
	v_mov_b64_e32 v[86:87], v[2:3]
	v_mfma_f32_16x16x128_f8f6f4 v[90:93], v[170:177], v[54:61], 0
	v_mfma_f32_16x16x128_f8f6f4 v[86:89], v[178:185], v[54:61], 0
	v_mov_b64_e32 v[60:61], v[4:5]
	v_mov_b64_e32 v[56:57], v[4:5]
	v_mov_b64_e32 v[28:29], v[4:5]
	v_mov_b64_e32 v[24:25], v[4:5]
	v_mov_b64_e32 v[12:13], v[4:5]
	v_mov_b64_e32 v[58:59], v[2:3]
	v_mov_b64_e32 v[54:55], v[2:3]
	v_mov_b64_e32 v[26:27], v[2:3]
	v_mov_b64_e32 v[22:23], v[2:3]
	v_mov_b64_e32 v[10:11], v[2:3]
	v_mfma_f32_16x16x128_f8f6f4 v[58:61], v[170:177], v[186:193], 0
	v_mfma_f32_16x16x128_f8f6f4 v[54:57], v[178:185], v[186:193], 0
	v_mfma_f32_16x16x128_f8f6f4 v[26:29], v[170:177], v[194:201], 0
	v_mfma_f32_16x16x128_f8f6f4 v[22:25], v[178:185], v[194:201], 0
	v_mfma_f32_16x16x128_f8f6f4 v[10:13], v[170:177], v[202:209], 0
	v_mfma_f32_16x16x128_f8f6f4 v[2:5], v[178:185], v[202:209], 0
	s_setprio 0
	s_barrier
	v_add_u32_e32 v170, s29, v210
	v_add_u32_e32 v171, s30, v210
	ds_read_b128 v[172:175], v170
	ds_read_b128 v[176:179], v170 offset:1024
	ds_read_b128 v[180:183], v170 offset:2048
	ds_read_b128 v[184:187], v170 offset:3072
	ds_read_b128 v[188:191], v171
	ds_read_b128 v[192:195], v171 offset:1024
	ds_read_b128 v[196:199], v171 offset:2048
	ds_read_b128 v[200:203], v171 offset:3072
	s_add_u32 s28, s8, 0x28100
	s_addc_u32 s29, s9, 0
	s_mov_b32 m0, s22
	v_lshl_add_u64 v[236:237], s[28:29], 0, v[162:163]
	ds_read_b128 v[204:207], v167 offset:32768
	ds_read_b128 v[208:211], v167 offset:33792
	ds_read_b128 v[212:215], v167 offset:34816
	ds_read_b128 v[216:219], v167 offset:35840
	ds_read_b128 v[220:223], v167 offset:36864
	ds_read_b128 v[224:227], v167 offset:37888
	ds_read_b128 v[228:231], v167 offset:38912
	ds_read_b128 v[232:235], v167 offset:39936
	global_load_lds_dwordx4 v[236:237], off
	v_lshl_add_u64 v[236:237], s[28:29], 0, v[148:149]
	s_mov_b32 m0, s23
	s_nop 0
	global_load_lds_dwordx4 v[236:237], off
	s_waitcnt vmcnt(8)
	s_waitcnt lgkmcnt(0)
	s_barrier
	s_setprio 1
	s_waitcnt lgkmcnt(0)
	v_mfma_f32_16x16x128_f8f6f4 v[122:125], v[172:179], v[204:211], v[122:125]
	v_mfma_f32_16x16x128_f8f6f4 v[114:117], v[180:187], v[204:211], v[114:117]
	v_mfma_f32_16x16x128_f8f6f4 v[106:109], v[172:179], v[212:219], v[106:109]
	v_mfma_f32_16x16x128_f8f6f4 v[98:101], v[180:187], v[212:219], v[98:101]
	v_mfma_f32_16x16x128_f8f6f4 v[74:77], v[172:179], v[220:227], v[74:77]
	v_mfma_f32_16x16x128_f8f6f4 v[66:69], v[180:187], v[220:227], v[66:69]
	v_mfma_f32_16x16x128_f8f6f4 v[42:45], v[172:179], v[228:235], v[42:45]
	v_mfma_f32_16x16x128_f8f6f4 v[34:37], v[180:187], v[228:235], v[34:37]
	s_setprio 0
	s_setprio 1
	v_mfma_f32_16x16x128_f8f6f4 v[126:129], v[188:195], v[204:211], v[126:129]
	v_mfma_f32_16x16x128_f8f6f4 v[118:121], v[196:203], v[204:211], v[118:121]
	v_mfma_f32_16x16x128_f8f6f4 v[110:113], v[188:195], v[212:219], v[110:113]
	v_mfma_f32_16x16x128_f8f6f4 v[102:105], v[196:203], v[212:219], v[102:105]
	v_mfma_f32_16x16x128_f8f6f4 v[78:81], v[188:195], v[220:227], v[78:81]
	v_mfma_f32_16x16x128_f8f6f4 v[70:73], v[196:203], v[220:227], v[70:73]
	v_mfma_f32_16x16x128_f8f6f4 v[46:49], v[188:195], v[228:235], v[46:49]
	v_mfma_f32_16x16x128_f8f6f4 v[38:41], v[196:203], v[228:235], v[38:41]
	s_setprio 0
	s_barrier
	s_mov_b64 s[28:29], 0x180
	s_mov_b32 m0, s16
	v_lshl_add_u64 v[236:237], v[158:159], 0, s[28:29]
	s_add_u32 s30, s10, 0x20180
	ds_read_b128 v[204:207], v167 offset:49152
	ds_read_b128 v[208:211], v167 offset:50176
	ds_read_b128 v[212:215], v167 offset:51200
	ds_read_b128 v[216:219], v167 offset:52224
	ds_read_b128 v[220:223], v167 offset:53248
	ds_read_b128 v[224:227], v167 offset:54272
	ds_read_b128 v[228:231], v167 offset:55296
	ds_read_b128 v[232:235], v167 offset:56320
	global_load_lds_dwordx4 v[236:237], off
	v_lshl_add_u64 v[236:237], v[160:161], 0, s[28:29]
	s_mov_b32 m0, s18
	s_addc_u32 s31, s11, 0
	global_load_lds_dwordx4 v[236:237], off
	v_lshl_add_u64 v[236:237], s[30:31], 0, v[130:131]
	s_mov_b32 m0, s20
	s_nop 0
	global_load_lds_dwordx4 v[236:237], off
	v_lshl_add_u64 v[236:237], s[30:31], 0, v[164:165]
	s_mov_b32 m0, s21
	s_nop 0
	global_load_lds_dwordx4 v[236:237], off
	v_lshl_add_u64 v[236:237], v[152:153], 0, s[28:29]
	s_mov_b32 m0, s17
	s_nop 0
	global_load_lds_dwordx4 v[236:237], off
	v_lshl_add_u64 v[236:237], v[154:155], 0, s[28:29]
	s_mov_b32 m0, s19
	s_nop 0
	global_load_lds_dwordx4 v[236:237], off
	s_waitcnt vmcnt(8)
	s_waitcnt lgkmcnt(0)
	s_barrier
	s_setprio 1
	s_waitcnt lgkmcnt(0)
	v_mfma_f32_16x16x128_f8f6f4 v[94:97], v[172:179], v[204:211], v[94:97]
	v_mfma_f32_16x16x128_f8f6f4 v[82:85], v[180:187], v[204:211], v[82:85]
	v_mfma_f32_16x16x128_f8f6f4 v[62:65], v[172:179], v[212:219], v[62:65]
	v_mfma_f32_16x16x128_f8f6f4 v[50:53], v[180:187], v[212:219], v[50:53]
	v_mfma_f32_16x16x128_f8f6f4 v[30:33], v[172:179], v[220:227], v[30:33]
	v_mfma_f32_16x16x128_f8f6f4 v[18:21], v[180:187], v[220:227], v[18:21]
	v_mfma_f32_16x16x128_f8f6f4 v[14:17], v[172:179], v[228:235], v[14:17]
	v_mfma_f32_16x16x128_f8f6f4 v[6:9], v[180:187], v[228:235], v[6:9]
	s_setprio 0
	s_setprio 1
	v_mfma_f32_16x16x128_f8f6f4 v[90:93], v[188:195], v[204:211], v[90:93]
	v_mfma_f32_16x16x128_f8f6f4 v[86:89], v[196:203], v[204:211], v[86:89]
	v_mfma_f32_16x16x128_f8f6f4 v[58:61], v[188:195], v[212:219], v[58:61]
	v_mfma_f32_16x16x128_f8f6f4 v[54:57], v[196:203], v[212:219], v[54:57]
	v_mfma_f32_16x16x128_f8f6f4 v[26:29], v[188:195], v[220:227], v[26:29]
	v_mfma_f32_16x16x128_f8f6f4 v[22:25], v[196:203], v[220:227], v[22:25]
	v_mfma_f32_16x16x128_f8f6f4 v[10:13], v[188:195], v[228:235], v[10:13]
	v_mfma_f32_16x16x128_f8f6f4 v[2:5], v[196:203], v[228:235], v[2:5]
	s_setprio 0
	s_barrier
	ds_read_b128 v[172:175], v168
	ds_read_b128 v[176:179], v168 offset:1024
	ds_read_b128 v[180:183], v168 offset:2048
	ds_read_b128 v[184:187], v168 offset:3072
	ds_read_b128 v[188:191], v169
	ds_read_b128 v[192:195], v169 offset:1024
	ds_read_b128 v[196:199], v169 offset:2048
	ds_read_b128 v[200:203], v169 offset:3072
	s_add_u32 s28, s8, 0x28180
	s_addc_u32 s29, s9, 0
	s_mov_b32 m0, s27
	v_lshl_add_u64 v[236:237], s[28:29], 0, v[162:163]
	ds_read_b128 v[204:207], v167
	ds_read_b128 v[208:211], v167 offset:1024
	ds_read_b128 v[212:215], v167 offset:2048
	ds_read_b128 v[216:219], v167 offset:3072
	ds_read_b128 v[220:223], v167 offset:4096
	ds_read_b128 v[224:227], v167 offset:5120
	ds_read_b128 v[228:231], v167 offset:6144
	ds_read_b128 v[232:235], v167 offset:7168
	global_load_lds_dwordx4 v[236:237], off
	v_lshl_add_u64 v[236:237], s[28:29], 0, v[148:149]
	s_mov_b32 m0, s26
	s_nop 0
	global_load_lds_dwordx4 v[236:237], off
	s_waitcnt vmcnt(8)
	s_waitcnt lgkmcnt(0)
	s_barrier
	s_setprio 1
	s_waitcnt lgkmcnt(0)
	v_mfma_f32_16x16x128_f8f6f4 v[122:125], v[172:179], v[204:211], v[122:125]
	v_mfma_f32_16x16x128_f8f6f4 v[114:117], v[180:187], v[204:211], v[114:117]
	v_mfma_f32_16x16x128_f8f6f4 v[106:109], v[172:179], v[212:219], v[106:109]
	v_mfma_f32_16x16x128_f8f6f4 v[98:101], v[180:187], v[212:219], v[98:101]
	v_mfma_f32_16x16x128_f8f6f4 v[74:77], v[172:179], v[220:227], v[74:77]
	v_mfma_f32_16x16x128_f8f6f4 v[66:69], v[180:187], v[220:227], v[66:69]
	v_mfma_f32_16x16x128_f8f6f4 v[42:45], v[172:179], v[228:235], v[42:45]
	v_mfma_f32_16x16x128_f8f6f4 v[34:37], v[180:187], v[228:235], v[34:37]
	s_setprio 0
	s_setprio 1
	v_mfma_f32_16x16x128_f8f6f4 v[126:129], v[188:195], v[204:211], v[126:129]
	v_mfma_f32_16x16x128_f8f6f4 v[118:121], v[196:203], v[204:211], v[118:121]
	v_mfma_f32_16x16x128_f8f6f4 v[110:113], v[188:195], v[212:219], v[110:113]
	v_mfma_f32_16x16x128_f8f6f4 v[102:105], v[196:203], v[212:219], v[102:105]
	v_mfma_f32_16x16x128_f8f6f4 v[78:81], v[188:195], v[220:227], v[78:81]
	v_mfma_f32_16x16x128_f8f6f4 v[70:73], v[196:203], v[220:227], v[70:73]
	v_mfma_f32_16x16x128_f8f6f4 v[46:49], v[188:195], v[228:235], v[46:49]
	v_mfma_f32_16x16x128_f8f6f4 v[38:41], v[196:203], v[228:235], v[38:41]
	s_setprio 0
	s_barrier
	s_mov_b64 s[28:29], 0x200
	s_mov_b32 m0, s4
	v_lshl_add_u64 v[236:237], v[158:159], 0, s[28:29]
	s_add_u32 s30, s10, 0x20200
	ds_read_b128 v[204:207], v167 offset:16384
	ds_read_b128 v[208:211], v167 offset:17408
	ds_read_b128 v[212:215], v167 offset:18432
	ds_read_b128 v[216:219], v167 offset:19456
	ds_read_b128 v[220:223], v167 offset:20480
	ds_read_b128 v[224:227], v167 offset:21504
	ds_read_b128 v[228:231], v167 offset:22528
	ds_read_b128 v[232:235], v167 offset:23552
	global_load_lds_dwordx4 v[236:237], off
	v_lshl_add_u64 v[236:237], v[160:161], 0, s[28:29]
	s_mov_b32 m0, s5
	s_addc_u32 s31, s11, 0
	global_load_lds_dwordx4 v[236:237], off
	v_lshl_add_u64 v[236:237], s[30:31], 0, v[130:131]
	s_mov_b32 m0, s6
	s_nop 0
	global_load_lds_dwordx4 v[236:237], off
	v_lshl_add_u64 v[236:237], s[30:31], 0, v[164:165]
	s_mov_b32 m0, s7
	s_nop 0
	global_load_lds_dwordx4 v[236:237], off
	v_lshl_add_u64 v[236:237], v[152:153], 0, s[28:29]
	s_mov_b32 m0, s24
	s_nop 0
	global_load_lds_dwordx4 v[236:237], off
	v_lshl_add_u64 v[236:237], v[154:155], 0, s[28:29]
	s_mov_b32 m0, s25
	s_nop 0
	global_load_lds_dwordx4 v[236:237], off
	s_waitcnt vmcnt(8)
	s_waitcnt lgkmcnt(0)
	s_barrier
	s_setprio 1
	s_waitcnt lgkmcnt(0)
	v_mfma_f32_16x16x128_f8f6f4 v[94:97], v[172:179], v[204:211], v[94:97]
	v_mfma_f32_16x16x128_f8f6f4 v[82:85], v[180:187], v[204:211], v[82:85]
	v_mfma_f32_16x16x128_f8f6f4 v[62:65], v[172:179], v[212:219], v[62:65]
	v_mfma_f32_16x16x128_f8f6f4 v[50:53], v[180:187], v[212:219], v[50:53]
	v_mfma_f32_16x16x128_f8f6f4 v[30:33], v[172:179], v[220:227], v[30:33]
	v_mfma_f32_16x16x128_f8f6f4 v[18:21], v[180:187], v[220:227], v[18:21]
	v_mfma_f32_16x16x128_f8f6f4 v[14:17], v[172:179], v[228:235], v[14:17]
	v_mfma_f32_16x16x128_f8f6f4 v[6:9], v[180:187], v[228:235], v[6:9]
	s_setprio 0
	s_setprio 1
	v_mfma_f32_16x16x128_f8f6f4 v[90:93], v[188:195], v[204:211], v[90:93]
	v_mfma_f32_16x16x128_f8f6f4 v[86:89], v[196:203], v[204:211], v[86:89]
	v_mfma_f32_16x16x128_f8f6f4 v[58:61], v[188:195], v[212:219], v[58:61]
	v_mfma_f32_16x16x128_f8f6f4 v[54:57], v[196:203], v[212:219], v[54:57]
	v_mfma_f32_16x16x128_f8f6f4 v[26:29], v[188:195], v[220:227], v[26:29]
	v_mfma_f32_16x16x128_f8f6f4 v[22:25], v[196:203], v[220:227], v[22:25]
	v_mfma_f32_16x16x128_f8f6f4 v[10:13], v[188:195], v[228:235], v[10:13]
	v_mfma_f32_16x16x128_f8f6f4 v[2:5], v[196:203], v[228:235], v[2:5]
	s_setprio 0
	s_barrier
	ds_read_b128 v[172:175], v170
	ds_read_b128 v[176:179], v170 offset:1024
	ds_read_b128 v[180:183], v170 offset:2048
	ds_read_b128 v[184:187], v170 offset:3072
	ds_read_b128 v[188:191], v171
	ds_read_b128 v[192:195], v171 offset:1024
	ds_read_b128 v[196:199], v171 offset:2048
	ds_read_b128 v[200:203], v171 offset:3072
	s_add_u32 s28, s8, 0x28200
	s_addc_u32 s29, s9, 0
	s_mov_b32 m0, s22
	v_lshl_add_u64 v[236:237], s[28:29], 0, v[162:163]
	ds_read_b128 v[204:207], v167 offset:32768
	ds_read_b128 v[208:211], v167 offset:33792
	ds_read_b128 v[212:215], v167 offset:34816
	ds_read_b128 v[216:219], v167 offset:35840
	ds_read_b128 v[220:223], v167 offset:36864
	ds_read_b128 v[224:227], v167 offset:37888
	ds_read_b128 v[228:231], v167 offset:38912
	ds_read_b128 v[232:235], v167 offset:39936
	global_load_lds_dwordx4 v[236:237], off
	v_lshl_add_u64 v[236:237], s[28:29], 0, v[148:149]
	s_mov_b32 m0, s23
	s_nop 0
	global_load_lds_dwordx4 v[236:237], off
	s_waitcnt vmcnt(8)
	s_waitcnt lgkmcnt(0)
	s_barrier
	s_setprio 1
	s_waitcnt lgkmcnt(0)
	v_mfma_f32_16x16x128_f8f6f4 v[122:125], v[172:179], v[204:211], v[122:125]
	v_mfma_f32_16x16x128_f8f6f4 v[114:117], v[180:187], v[204:211], v[114:117]
	v_mfma_f32_16x16x128_f8f6f4 v[106:109], v[172:179], v[212:219], v[106:109]
	v_mfma_f32_16x16x128_f8f6f4 v[98:101], v[180:187], v[212:219], v[98:101]
	v_mfma_f32_16x16x128_f8f6f4 v[74:77], v[172:179], v[220:227], v[74:77]
	v_mfma_f32_16x16x128_f8f6f4 v[66:69], v[180:187], v[220:227], v[66:69]
	v_mfma_f32_16x16x128_f8f6f4 v[42:45], v[172:179], v[228:235], v[42:45]
	v_mfma_f32_16x16x128_f8f6f4 v[34:37], v[180:187], v[228:235], v[34:37]
	s_setprio 0
	s_setprio 1
	v_mfma_f32_16x16x128_f8f6f4 v[126:129], v[188:195], v[204:211], v[126:129]
	v_mfma_f32_16x16x128_f8f6f4 v[118:121], v[196:203], v[204:211], v[118:121]
	v_mfma_f32_16x16x128_f8f6f4 v[110:113], v[188:195], v[212:219], v[110:113]
	v_mfma_f32_16x16x128_f8f6f4 v[102:105], v[196:203], v[212:219], v[102:105]
	v_mfma_f32_16x16x128_f8f6f4 v[78:81], v[188:195], v[220:227], v[78:81]
	v_mfma_f32_16x16x128_f8f6f4 v[70:73], v[196:203], v[220:227], v[70:73]
	v_mfma_f32_16x16x128_f8f6f4 v[46:49], v[188:195], v[228:235], v[46:49]
	v_mfma_f32_16x16x128_f8f6f4 v[38:41], v[196:203], v[228:235], v[38:41]
	s_setprio 0
	s_barrier
	s_mov_b64 s[28:29], 0x280
	s_mov_b32 m0, s16
	v_lshl_add_u64 v[236:237], v[158:159], 0, s[28:29]
	s_add_u32 s30, s10, 0x20280
	ds_read_b128 v[204:207], v167 offset:49152
	ds_read_b128 v[208:211], v167 offset:50176
	ds_read_b128 v[212:215], v167 offset:51200
	ds_read_b128 v[216:219], v167 offset:52224
	ds_read_b128 v[220:223], v167 offset:53248
	ds_read_b128 v[224:227], v167 offset:54272
	ds_read_b128 v[228:231], v167 offset:55296
	ds_read_b128 v[232:235], v167 offset:56320
	global_load_lds_dwordx4 v[236:237], off
	v_lshl_add_u64 v[236:237], v[160:161], 0, s[28:29]
	s_mov_b32 m0, s18
	s_addc_u32 s31, s11, 0
	global_load_lds_dwordx4 v[236:237], off
	v_lshl_add_u64 v[236:237], s[30:31], 0, v[130:131]
	s_mov_b32 m0, s20
	s_nop 0
	global_load_lds_dwordx4 v[236:237], off
	v_lshl_add_u64 v[236:237], s[30:31], 0, v[164:165]
	s_mov_b32 m0, s21
	s_nop 0
	global_load_lds_dwordx4 v[236:237], off
	v_lshl_add_u64 v[236:237], v[152:153], 0, s[28:29]
	s_mov_b32 m0, s17
	s_nop 0
	global_load_lds_dwordx4 v[236:237], off
	v_lshl_add_u64 v[236:237], v[154:155], 0, s[28:29]
	s_mov_b32 m0, s19
	s_nop 0
	global_load_lds_dwordx4 v[236:237], off
	s_waitcnt vmcnt(8)
	s_waitcnt lgkmcnt(0)
	s_barrier
	s_setprio 1
	s_waitcnt lgkmcnt(0)
	v_mfma_f32_16x16x128_f8f6f4 v[94:97], v[172:179], v[204:211], v[94:97]
	v_mfma_f32_16x16x128_f8f6f4 v[82:85], v[180:187], v[204:211], v[82:85]
	v_mfma_f32_16x16x128_f8f6f4 v[62:65], v[172:179], v[212:219], v[62:65]
	v_mfma_f32_16x16x128_f8f6f4 v[50:53], v[180:187], v[212:219], v[50:53]
	v_mfma_f32_16x16x128_f8f6f4 v[30:33], v[172:179], v[220:227], v[30:33]
	v_mfma_f32_16x16x128_f8f6f4 v[18:21], v[180:187], v[220:227], v[18:21]
	v_mfma_f32_16x16x128_f8f6f4 v[14:17], v[172:179], v[228:235], v[14:17]
	v_mfma_f32_16x16x128_f8f6f4 v[6:9], v[180:187], v[228:235], v[6:9]
	s_setprio 0
	s_setprio 1
	v_mfma_f32_16x16x128_f8f6f4 v[90:93], v[188:195], v[204:211], v[90:93]
	v_mfma_f32_16x16x128_f8f6f4 v[86:89], v[196:203], v[204:211], v[86:89]
	v_mfma_f32_16x16x128_f8f6f4 v[58:61], v[188:195], v[212:219], v[58:61]
	v_mfma_f32_16x16x128_f8f6f4 v[54:57], v[196:203], v[212:219], v[54:57]
	v_mfma_f32_16x16x128_f8f6f4 v[26:29], v[188:195], v[220:227], v[26:29]
	v_mfma_f32_16x16x128_f8f6f4 v[22:25], v[196:203], v[220:227], v[22:25]
	v_mfma_f32_16x16x128_f8f6f4 v[10:13], v[188:195], v[228:235], v[10:13]
	v_mfma_f32_16x16x128_f8f6f4 v[2:5], v[196:203], v[228:235], v[2:5]
	s_setprio 0
	s_barrier
	ds_read_b128 v[172:175], v168
	ds_read_b128 v[176:179], v168 offset:1024
	ds_read_b128 v[180:183], v168 offset:2048
	ds_read_b128 v[184:187], v168 offset:3072
	ds_read_b128 v[188:191], v169
	ds_read_b128 v[192:195], v169 offset:1024
	ds_read_b128 v[196:199], v169 offset:2048
	ds_read_b128 v[200:203], v169 offset:3072
	s_add_u32 s28, s8, 0x28280
	s_addc_u32 s29, s9, 0
	s_mov_b32 m0, s27
	v_lshl_add_u64 v[236:237], s[28:29], 0, v[162:163]
	ds_read_b128 v[204:207], v167
	ds_read_b128 v[208:211], v167 offset:1024
	ds_read_b128 v[212:215], v167 offset:2048
	ds_read_b128 v[216:219], v167 offset:3072
	ds_read_b128 v[220:223], v167 offset:4096
	ds_read_b128 v[224:227], v167 offset:5120
	ds_read_b128 v[228:231], v167 offset:6144
	ds_read_b128 v[232:235], v167 offset:7168
	global_load_lds_dwordx4 v[236:237], off
	v_lshl_add_u64 v[236:237], s[28:29], 0, v[148:149]
	s_mov_b32 m0, s26
	s_nop 0
	global_load_lds_dwordx4 v[236:237], off
	s_waitcnt vmcnt(8)
	s_waitcnt lgkmcnt(0)
	s_barrier
	s_setprio 1
	s_waitcnt lgkmcnt(0)
	v_mfma_f32_16x16x128_f8f6f4 v[122:125], v[172:179], v[204:211], v[122:125]
	v_mfma_f32_16x16x128_f8f6f4 v[114:117], v[180:187], v[204:211], v[114:117]
	v_mfma_f32_16x16x128_f8f6f4 v[106:109], v[172:179], v[212:219], v[106:109]
	v_mfma_f32_16x16x128_f8f6f4 v[98:101], v[180:187], v[212:219], v[98:101]
	v_mfma_f32_16x16x128_f8f6f4 v[74:77], v[172:179], v[220:227], v[74:77]
	v_mfma_f32_16x16x128_f8f6f4 v[66:69], v[180:187], v[220:227], v[66:69]
	v_mfma_f32_16x16x128_f8f6f4 v[42:45], v[172:179], v[228:235], v[42:45]
	v_mfma_f32_16x16x128_f8f6f4 v[34:37], v[180:187], v[228:235], v[34:37]
	s_setprio 0
	s_setprio 1
	v_mfma_f32_16x16x128_f8f6f4 v[126:129], v[188:195], v[204:211], v[126:129]
	v_mfma_f32_16x16x128_f8f6f4 v[118:121], v[196:203], v[204:211], v[118:121]
	v_mfma_f32_16x16x128_f8f6f4 v[110:113], v[188:195], v[212:219], v[110:113]
	v_mfma_f32_16x16x128_f8f6f4 v[102:105], v[196:203], v[212:219], v[102:105]
	v_mfma_f32_16x16x128_f8f6f4 v[78:81], v[188:195], v[220:227], v[78:81]
	v_mfma_f32_16x16x128_f8f6f4 v[70:73], v[196:203], v[220:227], v[70:73]
	v_mfma_f32_16x16x128_f8f6f4 v[46:49], v[188:195], v[228:235], v[46:49]
	v_mfma_f32_16x16x128_f8f6f4 v[38:41], v[196:203], v[228:235], v[38:41]
	s_setprio 0
	s_barrier
	s_mov_b64 s[28:29], 0x300
	s_mov_b32 m0, s4
	v_lshl_add_u64 v[236:237], v[158:159], 0, s[28:29]
	s_add_u32 s30, s10, 0x20300
	ds_read_b128 v[204:207], v167 offset:16384
	ds_read_b128 v[208:211], v167 offset:17408
	ds_read_b128 v[212:215], v167 offset:18432
	ds_read_b128 v[216:219], v167 offset:19456
	ds_read_b128 v[220:223], v167 offset:20480
	ds_read_b128 v[224:227], v167 offset:21504
	ds_read_b128 v[228:231], v167 offset:22528
	ds_read_b128 v[232:235], v167 offset:23552
	global_load_lds_dwordx4 v[236:237], off
	v_lshl_add_u64 v[236:237], v[160:161], 0, s[28:29]
	s_mov_b32 m0, s5
	s_addc_u32 s31, s11, 0
	global_load_lds_dwordx4 v[236:237], off
	v_lshl_add_u64 v[236:237], s[30:31], 0, v[130:131]
	s_mov_b32 m0, s6
	s_nop 0
	global_load_lds_dwordx4 v[236:237], off
	v_lshl_add_u64 v[236:237], s[30:31], 0, v[164:165]
	s_mov_b32 m0, s7
	s_nop 0
	global_load_lds_dwordx4 v[236:237], off
	v_lshl_add_u64 v[236:237], v[152:153], 0, s[28:29]
	s_mov_b32 m0, s24
	s_nop 0
	global_load_lds_dwordx4 v[236:237], off
	v_lshl_add_u64 v[236:237], v[154:155], 0, s[28:29]
	s_mov_b32 m0, s25
	s_nop 0
	global_load_lds_dwordx4 v[236:237], off
	s_waitcnt vmcnt(8)
	s_waitcnt lgkmcnt(0)
	s_barrier
	s_setprio 1
	s_waitcnt lgkmcnt(0)
	v_mfma_f32_16x16x128_f8f6f4 v[94:97], v[172:179], v[204:211], v[94:97]
	v_mfma_f32_16x16x128_f8f6f4 v[82:85], v[180:187], v[204:211], v[82:85]
	v_mfma_f32_16x16x128_f8f6f4 v[62:65], v[172:179], v[212:219], v[62:65]
	v_mfma_f32_16x16x128_f8f6f4 v[50:53], v[180:187], v[212:219], v[50:53]
	v_mfma_f32_16x16x128_f8f6f4 v[30:33], v[172:179], v[220:227], v[30:33]
	v_mfma_f32_16x16x128_f8f6f4 v[18:21], v[180:187], v[220:227], v[18:21]
	v_mfma_f32_16x16x128_f8f6f4 v[14:17], v[172:179], v[228:235], v[14:17]
	v_mfma_f32_16x16x128_f8f6f4 v[6:9], v[180:187], v[228:235], v[6:9]
	s_setprio 0
	s_setprio 1
	v_mfma_f32_16x16x128_f8f6f4 v[90:93], v[188:195], v[204:211], v[90:93]
	v_mfma_f32_16x16x128_f8f6f4 v[86:89], v[196:203], v[204:211], v[86:89]
	v_mfma_f32_16x16x128_f8f6f4 v[58:61], v[188:195], v[212:219], v[58:61]
	v_mfma_f32_16x16x128_f8f6f4 v[54:57], v[196:203], v[212:219], v[54:57]
	v_mfma_f32_16x16x128_f8f6f4 v[26:29], v[188:195], v[220:227], v[26:29]
	v_mfma_f32_16x16x128_f8f6f4 v[22:25], v[196:203], v[220:227], v[22:25]
	v_mfma_f32_16x16x128_f8f6f4 v[10:13], v[188:195], v[228:235], v[10:13]
	v_mfma_f32_16x16x128_f8f6f4 v[2:5], v[196:203], v[228:235], v[2:5]
	s_setprio 0
	s_barrier
	ds_read_b128 v[172:175], v170
	ds_read_b128 v[176:179], v170 offset:1024
	ds_read_b128 v[180:183], v170 offset:2048
	ds_read_b128 v[184:187], v170 offset:3072
	ds_read_b128 v[188:191], v171
	ds_read_b128 v[192:195], v171 offset:1024
	ds_read_b128 v[196:199], v171 offset:2048
	ds_read_b128 v[200:203], v171 offset:3072
	s_add_u32 s28, s8, 0x28300
	s_addc_u32 s29, s9, 0
	s_mov_b32 m0, s22
	v_lshl_add_u64 v[236:237], s[28:29], 0, v[162:163]
	ds_read_b128 v[204:207], v167 offset:32768
	ds_read_b128 v[208:211], v167 offset:33792
	ds_read_b128 v[212:215], v167 offset:34816
	ds_read_b128 v[216:219], v167 offset:35840
	ds_read_b128 v[220:223], v167 offset:36864
	ds_read_b128 v[224:227], v167 offset:37888
	ds_read_b128 v[228:231], v167 offset:38912
	ds_read_b128 v[232:235], v167 offset:39936
	global_load_lds_dwordx4 v[236:237], off
	v_lshl_add_u64 v[236:237], s[28:29], 0, v[148:149]
	s_mov_b32 m0, s23
	s_nop 0
	global_load_lds_dwordx4 v[236:237], off
	s_waitcnt vmcnt(8)
	s_waitcnt lgkmcnt(0)
	s_barrier
	s_setprio 1
	s_waitcnt lgkmcnt(0)
	v_mfma_f32_16x16x128_f8f6f4 v[122:125], v[172:179], v[204:211], v[122:125]
	v_mfma_f32_16x16x128_f8f6f4 v[114:117], v[180:187], v[204:211], v[114:117]
	v_mfma_f32_16x16x128_f8f6f4 v[106:109], v[172:179], v[212:219], v[106:109]
	v_mfma_f32_16x16x128_f8f6f4 v[98:101], v[180:187], v[212:219], v[98:101]
	v_mfma_f32_16x16x128_f8f6f4 v[74:77], v[172:179], v[220:227], v[74:77]
	v_mfma_f32_16x16x128_f8f6f4 v[66:69], v[180:187], v[220:227], v[66:69]
	v_mfma_f32_16x16x128_f8f6f4 v[42:45], v[172:179], v[228:235], v[42:45]
	v_mfma_f32_16x16x128_f8f6f4 v[34:37], v[180:187], v[228:235], v[34:37]
	s_setprio 0
	s_setprio 1
	v_mfma_f32_16x16x128_f8f6f4 v[126:129], v[188:195], v[204:211], v[126:129]
	v_mfma_f32_16x16x128_f8f6f4 v[118:121], v[196:203], v[204:211], v[118:121]
	v_mfma_f32_16x16x128_f8f6f4 v[110:113], v[188:195], v[212:219], v[110:113]
	v_mfma_f32_16x16x128_f8f6f4 v[102:105], v[196:203], v[212:219], v[102:105]
	v_mfma_f32_16x16x128_f8f6f4 v[78:81], v[188:195], v[220:227], v[78:81]
	v_mfma_f32_16x16x128_f8f6f4 v[70:73], v[196:203], v[220:227], v[70:73]
	v_mfma_f32_16x16x128_f8f6f4 v[46:49], v[188:195], v[228:235], v[46:49]
	v_mfma_f32_16x16x128_f8f6f4 v[38:41], v[196:203], v[228:235], v[38:41]
	s_setprio 0
	s_barrier
	s_mov_b64 s[28:29], 0x380
	s_mov_b32 m0, s16
	v_lshl_add_u64 v[236:237], v[158:159], 0, s[28:29]
	s_add_u32 s10, s10, 0x20380
	ds_read_b128 v[204:207], v167 offset:49152
	ds_read_b128 v[208:211], v167 offset:50176
	ds_read_b128 v[212:215], v167 offset:51200
	ds_read_b128 v[216:219], v167 offset:52224
	ds_read_b128 v[220:223], v167 offset:53248
	ds_read_b128 v[224:227], v167 offset:54272
	ds_read_b128 v[228:231], v167 offset:55296
	ds_read_b128 v[232:235], v167 offset:56320
	global_load_lds_dwordx4 v[236:237], off
	v_lshl_add_u64 v[236:237], v[160:161], 0, s[28:29]
	s_mov_b32 m0, s18
	s_addc_u32 s11, s11, 0
	global_load_lds_dwordx4 v[236:237], off
	v_lshl_add_u64 v[236:237], s[10:11], 0, v[130:131]
	s_mov_b32 m0, s20
	v_lshl_add_u64 v[164:165], s[10:11], 0, v[164:165]
	global_load_lds_dwordx4 v[236:237], off
	s_mov_b32 m0, s21
	s_nop 0
	global_load_lds_dwordx4 v[164:165], off
	v_lshl_add_u64 v[164:165], v[152:153], 0, s[28:29]
	s_mov_b32 m0, s17
	s_nop 0
	global_load_lds_dwordx4 v[164:165], off
	v_lshl_add_u64 v[164:165], v[154:155], 0, s[28:29]
	s_mov_b32 m0, s19
	s_nop 0
	global_load_lds_dwordx4 v[164:165], off
	s_waitcnt vmcnt(8)
	s_waitcnt lgkmcnt(0)
	s_barrier
	s_setprio 1
	s_waitcnt lgkmcnt(0)
	v_mfma_f32_16x16x128_f8f6f4 v[94:97], v[172:179], v[204:211], v[94:97]
	v_mfma_f32_16x16x128_f8f6f4 v[82:85], v[180:187], v[204:211], v[82:85]
	v_mfma_f32_16x16x128_f8f6f4 v[62:65], v[172:179], v[212:219], v[62:65]
	v_mfma_f32_16x16x128_f8f6f4 v[50:53], v[180:187], v[212:219], v[50:53]
	v_mfma_f32_16x16x128_f8f6f4 v[30:33], v[172:179], v[220:227], v[30:33]
	v_mfma_f32_16x16x128_f8f6f4 v[18:21], v[180:187], v[220:227], v[18:21]
	v_mfma_f32_16x16x128_f8f6f4 v[14:17], v[172:179], v[228:235], v[14:17]
	v_mfma_f32_16x16x128_f8f6f4 v[6:9], v[180:187], v[228:235], v[6:9]
	s_setprio 0
	s_setprio 1
	v_mfma_f32_16x16x128_f8f6f4 v[90:93], v[188:195], v[204:211], v[90:93]
	v_mfma_f32_16x16x128_f8f6f4 v[86:89], v[196:203], v[204:211], v[86:89]
	v_mfma_f32_16x16x128_f8f6f4 v[58:61], v[188:195], v[212:219], v[58:61]
	v_mfma_f32_16x16x128_f8f6f4 v[54:57], v[196:203], v[212:219], v[54:57]
	v_mfma_f32_16x16x128_f8f6f4 v[26:29], v[188:195], v[220:227], v[26:29]
	v_mfma_f32_16x16x128_f8f6f4 v[22:25], v[196:203], v[220:227], v[22:25]
	v_mfma_f32_16x16x128_f8f6f4 v[10:13], v[188:195], v[228:235], v[10:13]
	v_mfma_f32_16x16x128_f8f6f4 v[2:5], v[196:203], v[228:235], v[2:5]
	s_setprio 0
	s_barrier
	ds_read_b128 v[172:175], v168
	ds_read_b128 v[176:179], v168 offset:1024
	ds_read_b128 v[180:183], v168 offset:2048
	ds_read_b128 v[184:187], v168 offset:3072
	ds_read_b128 v[188:191], v169
	ds_read_b128 v[192:195], v169 offset:1024
	ds_read_b128 v[196:199], v169 offset:2048
	ds_read_b128 v[200:203], v169 offset:3072
	s_add_u32 s8, s8, 0x28380
	s_addc_u32 s9, s9, 0
	s_mov_b32 m0, s27
	v_lshl_add_u64 v[162:163], s[8:9], 0, v[162:163]
	ds_read_b128 v[204:207], v167
	ds_read_b128 v[208:211], v167 offset:1024
	ds_read_b128 v[212:215], v167 offset:2048
	ds_read_b128 v[216:219], v167 offset:3072
	ds_read_b128 v[220:223], v167 offset:4096
	ds_read_b128 v[224:227], v167 offset:5120
	ds_read_b128 v[228:231], v167 offset:6144
	ds_read_b128 v[232:235], v167 offset:7168
	global_load_lds_dwordx4 v[162:163], off
	v_lshl_add_u64 v[148:149], s[8:9], 0, v[148:149]
	s_mov_b32 m0, s26
	s_nop 0
	global_load_lds_dwordx4 v[148:149], off
	s_waitcnt vmcnt(8)
	s_waitcnt lgkmcnt(0)
	s_barrier
	s_setprio 1
	s_waitcnt lgkmcnt(0)
	v_mfma_f32_16x16x128_f8f6f4 v[122:125], v[172:179], v[204:211], v[122:125]
	v_mfma_f32_16x16x128_f8f6f4 v[114:117], v[180:187], v[204:211], v[114:117]
	v_mfma_f32_16x16x128_f8f6f4 v[106:109], v[172:179], v[212:219], v[106:109]
	v_mfma_f32_16x16x128_f8f6f4 v[98:101], v[180:187], v[212:219], v[98:101]
	v_mfma_f32_16x16x128_f8f6f4 v[74:77], v[172:179], v[220:227], v[74:77]
	v_mfma_f32_16x16x128_f8f6f4 v[66:69], v[180:187], v[220:227], v[66:69]
	v_mfma_f32_16x16x128_f8f6f4 v[42:45], v[172:179], v[228:235], v[42:45]
	v_mfma_f32_16x16x128_f8f6f4 v[34:37], v[180:187], v[228:235], v[34:37]
	s_setprio 0
	s_setprio 1
	v_mfma_f32_16x16x128_f8f6f4 v[126:129], v[188:195], v[204:211], v[126:129]
	v_mfma_f32_16x16x128_f8f6f4 v[118:121], v[196:203], v[204:211], v[118:121]
	v_mfma_f32_16x16x128_f8f6f4 v[110:113], v[188:195], v[212:219], v[110:113]
	v_mfma_f32_16x16x128_f8f6f4 v[102:105], v[196:203], v[212:219], v[102:105]
	v_mfma_f32_16x16x128_f8f6f4 v[78:81], v[188:195], v[220:227], v[78:81]
	v_mfma_f32_16x16x128_f8f6f4 v[70:73], v[196:203], v[220:227], v[70:73]
	v_mfma_f32_16x16x128_f8f6f4 v[46:49], v[188:195], v[228:235], v[46:49]
	v_mfma_f32_16x16x128_f8f6f4 v[38:41], v[196:203], v[228:235], v[38:41]
	s_setprio 0
	s_barrier
	s_mov_b32 m0, s4
	ds_read_b128 v[204:207], v167 offset:16384
	ds_read_b128 v[208:211], v167 offset:17408
	ds_read_b128 v[212:215], v167 offset:18432
	ds_read_b128 v[216:219], v167 offset:19456
	ds_read_b128 v[220:223], v167 offset:20480
	ds_read_b128 v[224:227], v167 offset:21504
	ds_read_b128 v[228:231], v167 offset:22528
	ds_read_b128 v[232:235], v167 offset:23552
	global_load_lds_dwordx4 v[158:159], off
	s_mov_b32 m0, s5
	s_nop 0
	global_load_lds_dwordx4 v[160:161], off
	s_mov_b32 m0, s6
	s_nop 0
	global_load_lds_dwordx4 v[156:157], off
	s_mov_b32 m0, s7
	s_nop 0
	global_load_lds_dwordx4 v[150:151], off
	s_mov_b32 m0, s24
	s_nop 0
	global_load_lds_dwordx4 v[152:153], off
	s_mov_b32 m0, s25
	s_nop 0
	global_load_lds_dwordx4 v[154:155], off
	s_waitcnt vmcnt(8)
	s_waitcnt lgkmcnt(0)
	s_barrier
	s_setprio 1
	s_waitcnt lgkmcnt(0)
	v_mfma_f32_16x16x128_f8f6f4 v[94:97], v[172:179], v[204:211], v[94:97]
	v_mfma_f32_16x16x128_f8f6f4 v[82:85], v[180:187], v[204:211], v[82:85]
	v_mfma_f32_16x16x128_f8f6f4 v[62:65], v[172:179], v[212:219], v[62:65]
	v_mfma_f32_16x16x128_f8f6f4 v[50:53], v[180:187], v[212:219], v[50:53]
	v_mfma_f32_16x16x128_f8f6f4 v[30:33], v[172:179], v[220:227], v[30:33]
	v_mfma_f32_16x16x128_f8f6f4 v[18:21], v[180:187], v[220:227], v[18:21]
	v_mfma_f32_16x16x128_f8f6f4 v[14:17], v[172:179], v[228:235], v[14:17]
	v_mfma_f32_16x16x128_f8f6f4 v[6:9], v[180:187], v[228:235], v[6:9]
	s_setprio 0
	s_setprio 1
	v_mfma_f32_16x16x128_f8f6f4 v[90:93], v[188:195], v[204:211], v[90:93]
	v_mfma_f32_16x16x128_f8f6f4 v[86:89], v[196:203], v[204:211], v[86:89]
	v_mfma_f32_16x16x128_f8f6f4 v[58:61], v[188:195], v[212:219], v[58:61]
	v_mfma_f32_16x16x128_f8f6f4 v[54:57], v[196:203], v[212:219], v[54:57]
	v_mfma_f32_16x16x128_f8f6f4 v[26:29], v[188:195], v[220:227], v[26:29]
	v_mfma_f32_16x16x128_f8f6f4 v[22:25], v[196:203], v[220:227], v[22:25]
	v_mfma_f32_16x16x128_f8f6f4 v[10:13], v[188:195], v[228:235], v[10:13]
	v_mfma_f32_16x16x128_f8f6f4 v[2:5], v[196:203], v[228:235], v[2:5]
	s_setprio 0
	s_barrier
	ds_read_b128 v[148:151], v170
	ds_read_b128 v[152:155], v170 offset:1024
	ds_read_b128 v[156:159], v170 offset:2048
	ds_read_b128 v[160:163], v170 offset:3072
	ds_read_b128 v[172:175], v171
	ds_read_b128 v[176:179], v171 offset:1024
	ds_read_b128 v[180:183], v171 offset:2048
	ds_read_b128 v[184:187], v171 offset:3072
	s_mov_b32 m0, s22
	ds_read_b128 v[188:191], v167 offset:32768
	ds_read_b128 v[192:195], v167 offset:33792
	ds_read_b128 v[196:199], v167 offset:34816
	ds_read_b128 v[200:203], v167 offset:35840
	ds_read_b128 v[204:207], v167 offset:36864
	ds_read_b128 v[208:211], v167 offset:37888
	ds_read_b128 v[212:215], v167 offset:38912
	ds_read_b128 v[216:219], v167 offset:39936
	global_load_lds_dwordx4 v[144:145], off
	s_mov_b32 m0, s23
	s_nop 0
	global_load_lds_dwordx4 v[146:147], off
	s_waitcnt vmcnt(8)
	s_waitcnt lgkmcnt(0)
	s_barrier
	s_setprio 1
	s_waitcnt lgkmcnt(0)
	v_mfma_f32_16x16x128_f8f6f4 v[122:125], v[148:155], v[188:195], v[122:125]
	v_mfma_f32_16x16x128_f8f6f4 v[114:117], v[156:163], v[188:195], v[114:117]
	v_mfma_f32_16x16x128_f8f6f4 v[106:109], v[148:155], v[196:203], v[106:109]
	v_mfma_f32_16x16x128_f8f6f4 v[98:101], v[156:163], v[196:203], v[98:101]
	v_mfma_f32_16x16x128_f8f6f4 v[74:77], v[148:155], v[204:211], v[74:77]
	v_mfma_f32_16x16x128_f8f6f4 v[66:69], v[156:163], v[204:211], v[66:69]
	v_mfma_f32_16x16x128_f8f6f4 v[42:45], v[148:155], v[212:219], v[42:45]
	v_mfma_f32_16x16x128_f8f6f4 v[34:37], v[156:163], v[212:219], v[34:37]
	s_setprio 0
	s_setprio 1
	v_mfma_f32_16x16x128_f8f6f4 v[126:129], v[172:179], v[188:195], v[126:129]
	v_mfma_f32_16x16x128_f8f6f4 v[118:121], v[180:187], v[188:195], v[118:121]
	v_mfma_f32_16x16x128_f8f6f4 v[110:113], v[172:179], v[196:203], v[110:113]
	v_mfma_f32_16x16x128_f8f6f4 v[102:105], v[180:187], v[196:203], v[102:105]
	v_mfma_f32_16x16x128_f8f6f4 v[78:81], v[172:179], v[204:211], v[78:81]
	v_mfma_f32_16x16x128_f8f6f4 v[70:73], v[180:187], v[204:211], v[70:73]
	v_mfma_f32_16x16x128_f8f6f4 v[46:49], v[172:179], v[212:219], v[46:49]
	v_mfma_f32_16x16x128_f8f6f4 v[38:41], v[180:187], v[212:219], v[38:41]
	s_setprio 0
	s_barrier
	s_mov_b32 m0, s16
	ds_read_b128 v[188:191], v167 offset:49152
	ds_read_b128 v[192:195], v167 offset:50176
	ds_read_b128 v[196:199], v167 offset:51200
	ds_read_b128 v[200:203], v167 offset:52224
	ds_read_b128 v[204:207], v167 offset:53248
	ds_read_b128 v[208:211], v167 offset:54272
	ds_read_b128 v[212:215], v167 offset:55296
	ds_read_b128 v[216:219], v167 offset:56320
	global_load_lds_dwordx4 v[134:135], off
	s_mov_b32 m0, s18
	s_nop 0
	global_load_lds_dwordx4 v[136:137], off
	s_mov_b32 m0, s20
	s_nop 0
	global_load_lds_dwordx4 v[140:141], off
	s_mov_b32 m0, s21
	s_nop 0
	global_load_lds_dwordx4 v[142:143], off
	s_mov_b32 m0, s17
	s_nop 0
	global_load_lds_dwordx4 v[132:133], off
	s_mov_b32 m0, s19
	s_nop 0
	global_load_lds_dwordx4 v[138:139], off
	s_waitcnt vmcnt(8)
	s_waitcnt lgkmcnt(0)
	s_barrier
	s_setprio 1
	s_waitcnt lgkmcnt(0)
	v_mfma_f32_16x16x128_f8f6f4 v[94:97], v[148:155], v[188:195], v[94:97]
	v_mfma_f32_16x16x128_f8f6f4 v[82:85], v[156:163], v[188:195], v[82:85]
	v_mfma_f32_16x16x128_f8f6f4 v[62:65], v[148:155], v[196:203], v[62:65]
	v_mfma_f32_16x16x128_f8f6f4 v[50:53], v[156:163], v[196:203], v[50:53]
	v_mfma_f32_16x16x128_f8f6f4 v[30:33], v[148:155], v[204:211], v[30:33]
	v_mfma_f32_16x16x128_f8f6f4 v[18:21], v[156:163], v[204:211], v[18:21]
	v_mfma_f32_16x16x128_f8f6f4 v[14:17], v[148:155], v[212:219], v[14:17]
	v_mfma_f32_16x16x128_f8f6f4 v[6:9], v[156:163], v[212:219], v[6:9]
	s_setprio 0
	s_setprio 1
	v_mfma_f32_16x16x128_f8f6f4 v[90:93], v[172:179], v[188:195], v[90:93]
	v_mfma_f32_16x16x128_f8f6f4 v[86:89], v[180:187], v[188:195], v[86:89]
	v_mfma_f32_16x16x128_f8f6f4 v[58:61], v[172:179], v[196:203], v[58:61]
	v_mfma_f32_16x16x128_f8f6f4 v[54:57], v[180:187], v[196:203], v[54:57]
	v_mfma_f32_16x16x128_f8f6f4 v[26:29], v[172:179], v[204:211], v[26:29]
	v_mfma_f32_16x16x128_f8f6f4 v[22:25], v[180:187], v[204:211], v[22:25]
	v_mfma_f32_16x16x128_f8f6f4 v[10:13], v[172:179], v[212:219], v[10:13]
	v_mfma_f32_16x16x128_f8f6f4 v[2:5], v[180:187], v[212:219], v[2:5]
	s_setprio 0
	s_barrier
; #define GAS __attribute__((address_space(1)))
;     __device__ __forceinline__ void operator()(const f32x4 (&acc)[2][2][4][2], const Unit& u, int wr, int wc, int fr, int fq) const {
;         float* base = C + (size_t)u.aux * cstride; const int row0 = u.pm * 256 + wr * 64 + fr, col0 = u.pn * 256 + wc * 32 + 4 * fq;
; #pragma unroll
;         for (int ai = 0; ai < 2; ++ai)
; #pragma unroll
;             for (int m = 0; m < 4; ++m) { float* rowp = base + (size_t)(row0 + ai * 128 + m * 16) * ldc + col0;
; #pragma unroll
;                 for (int bj = 0; bj < 2; ++bj)
; #pragma unroll
;                     for (int n = 0; n < 2; ++n) *(GAS f32x4*)(rowp + bj * 128 + n * 16) = acc[ai][bj][m][n] * scale; }
	s_lshl_b64 s[2:3], s[2:3], 19
	s_add_u32 s2, s33, s2
	s_addc_u32 s3, s40, s3
	v_add_u32_e32 v132, s1, v166
	v_lshl_or_b32 v130, s15, 2, v1
	v_lshl_add_u64 v[130:131], s[2:3], 0, v[130:131]
	s_mov_b64 s[2:3], 0x56900000
	v_ashrrev_i32_e32 v133, 31, v132
	v_lshl_add_u64 v[134:135], v[130:131], 0, s[2:3]
	v_lshlrev_b64 v[130:131], 10, v[132:133]
	s_mov_b32 s2, 0x38800000
	v_lshl_add_u64 v[130:131], v[134:135], 0, v[130:131]
	v_pk_mul_f32 v[116:117], v[116:117], s[2:3] op_sel_hi:[1,0]
	v_pk_mul_f32 v[114:115], v[114:115], s[2:3] op_sel_hi:[1,0]
	s_nop 15
	s_nop 7
	global_store_dwordx4 v[130:131], v[114:117], off offset:64 sc1
	v_pk_mul_f32 v[100:101], v[100:101], s[2:3] op_sel_hi:[1,0]
	v_pk_mul_f32 v[98:99], v[98:99], s[2:3] op_sel_hi:[1,0]
	v_pk_mul_f32 v[116:117], v[128:129], s[2:3] op_sel_hi:[1,0]
	v_pk_mul_f32 v[114:115], v[126:127], s[2:3] op_sel_hi:[1,0]
	global_store_dwordx4 v[130:131], v[114:117], off offset:512 sc1
	v_pk_mul_f32 v[68:69], v[68:69], s[2:3] op_sel_hi:[1,0]
	v_pk_mul_f32 v[66:67], v[66:67], s[2:3] op_sel_hi:[1,0]
	v_pk_mul_f32 v[116:117], v[120:121], s[2:3] op_sel_hi:[1,0]
	v_pk_mul_f32 v[114:115], v[118:119], s[2:3] op_sel_hi:[1,0]
	global_store_dwordx4 v[130:131], v[114:117], off offset:576 sc1
	v_pk_mul_f32 v[36:37], v[36:37], s[2:3] op_sel_hi:[1,0]
	v_pk_mul_f32 v[34:35], v[34:35], s[2:3] op_sel_hi:[1,0]
	v_or_b32_e32 v114, 16, v132
	v_ashrrev_i32_e32 v115, 31, v114
	v_lshlrev_b64 v[114:115], 10, v[114:115]
	v_lshl_add_u64 v[114:115], v[134:135], 0, v[114:115]
	global_store_dwordx4 v[114:115], v[98:101], off offset:64 sc1
	s_mov_b32 s1, 0x20000
	s_mov_b64 s[4:5], 0x20000
	v_pk_mul_f32 v[100:101], v[112:113], s[2:3] op_sel_hi:[1,0]
	v_pk_mul_f32 v[98:99], v[110:111], s[2:3] op_sel_hi:[1,0]
	global_store_dwordx4 v[114:115], v[98:101], off offset:512 sc1
	v_pk_mul_f32 v[20:21], v[20:21], s[2:3] op_sel_hi:[1,0]
	v_pk_mul_f32 v[18:19], v[18:19], s[2:3] op_sel_hi:[1,0]
	v_pk_mul_f32 v[100:101], v[104:105], s[2:3] op_sel_hi:[1,0]
	v_pk_mul_f32 v[98:99], v[102:103], s[2:3] op_sel_hi:[1,0]
	global_store_dwordx4 v[114:115], v[98:101], off offset:576 sc1
	v_pk_mul_f32 v[8:9], v[8:9], s[2:3] op_sel_hi:[1,0]
	v_pk_mul_f32 v[6:7], v[6:7], s[2:3] op_sel_hi:[1,0]
	v_or_b32_e32 v98, 32, v132
	v_ashrrev_i32_e32 v99, 31, v98
	v_lshlrev_b64 v[98:99], 10, v[98:99]
	v_lshl_add_u64 v[98:99], v[134:135], 0, v[98:99]
	global_store_dwordx4 v[98:99], v[66:69], off offset:64 sc1
	v_pk_mul_f32 v[124:125], v[124:125], s[2:3] op_sel_hi:[1,0]
	v_pk_mul_f32 v[122:123], v[122:123], s[2:3] op_sel_hi:[1,0]
	v_pk_mul_f32 v[68:69], v[80:81], s[2:3] op_sel_hi:[1,0]
	v_pk_mul_f32 v[66:67], v[78:79], s[2:3] op_sel_hi:[1,0]
	global_store_dwordx4 v[98:99], v[66:69], off offset:512 sc1
	v_pk_mul_f32 v[108:109], v[108:109], s[2:3] op_sel_hi:[1,0]
	v_pk_mul_f32 v[106:107], v[106:107], s[2:3] op_sel_hi:[1,0]
	v_pk_mul_f32 v[68:69], v[72:73], s[2:3] op_sel_hi:[1,0]
	v_pk_mul_f32 v[66:67], v[70:71], s[2:3] op_sel_hi:[1,0]
	global_store_dwordx4 v[98:99], v[66:69], off offset:576 sc1
	v_pk_mul_f32 v[76:77], v[76:77], s[2:3] op_sel_hi:[1,0]
	v_pk_mul_f32 v[74:75], v[74:75], s[2:3] op_sel_hi:[1,0]
	v_or_b32_e32 v66, 48, v132
	v_ashrrev_i32_e32 v67, 31, v66
	v_lshlrev_b64 v[66:67], 10, v[66:67]
	v_lshl_add_u64 v[66:67], v[134:135], 0, v[66:67]
	global_store_dwordx4 v[66:67], v[34:37], off offset:64 sc1
	v_pk_mul_f32 v[44:45], v[44:45], s[2:3] op_sel_hi:[1,0]
	v_pk_mul_f32 v[42:43], v[42:43], s[2:3] op_sel_hi:[1,0]
	v_pk_mul_f32 v[36:37], v[48:49], s[2:3] op_sel_hi:[1,0]
	v_pk_mul_f32 v[34:35], v[46:47], s[2:3] op_sel_hi:[1,0]
	global_store_dwordx4 v[66:67], v[34:37], off offset:512 sc1
; #define GAS __attribute__((address_space(1)))
;     __device__ __forceinline__ void operator()(const f32x4 (&acc)[2][2][4][2], const Unit& u, int wr, int wc, int fr, int fq) const {
;         float* base = C + (size_t)u.aux * cstride; const int row0 = u.pm * 256 + wr * 64 + fr, col0 = u.pn * 256 + wc * 32 + 4 * fq;
; #pragma unroll
;         for (int ai = 0; ai < 2; ++ai)
; #pragma unroll
;             for (int m = 0; m < 4; ++m) { float* rowp = base + (size_t)(row0 + ai * 128 + m * 16) * ldc + col0;
; #pragma unroll
;                 for (int bj = 0; bj < 2; ++bj)
; #pragma unroll
;                     for (int n = 0; n < 2; ++n) *(GAS f32x4*)(rowp + bj * 128 + n * 16) = acc[ai][bj][m][n] * scale; }
	v_pk_mul_f32 v[32:33], v[32:33], s[2:3] op_sel_hi:[1,0]
	v_pk_mul_f32 v[30:31], v[30:31], s[2:3] op_sel_hi:[1,0]
	v_pk_mul_f32 v[36:37], v[40:41], s[2:3] op_sel_hi:[1,0]
	v_pk_mul_f32 v[34:35], v[38:39], s[2:3] op_sel_hi:[1,0]
	v_add_co_u32_e32 v40, vcc, s1, v130
	global_store_dwordx4 v[66:67], v[34:37], off offset:576 sc1
	s_nop 0
	v_addc_co_u32_e32 v41, vcc, 0, v131, vcc
	v_pk_mul_f32 v[36:37], v[96:97], s[2:3] op_sel_hi:[1,0]
	v_pk_mul_f32 v[34:35], v[94:95], s[2:3] op_sel_hi:[1,0]
	v_lshl_add_u64 v[38:39], v[130:131], 0, s[4:5]
	global_store_dwordx4 v[40:41], v[34:37], off sc1
	s_mov_b32 s1, 0x24000
	v_add_co_u32_e32 v40, vcc, s1, v130
	v_pk_mul_f32 v[36:37], v[84:85], s[2:3] op_sel_hi:[1,0]
	v_pk_mul_f32 v[34:35], v[82:83], s[2:3] op_sel_hi:[1,0]
	global_store_dwordx4 v[38:39], v[34:37], off offset:64 sc1
	s_mov_b64 s[4:5], 0x24000
	v_addc_co_u32_e32 v41, vcc, 0, v131, vcc
	v_pk_mul_f32 v[36:37], v[92:93], s[2:3] op_sel_hi:[1,0]
	v_pk_mul_f32 v[34:35], v[90:91], s[2:3] op_sel_hi:[1,0]
	global_store_dwordx4 v[38:39], v[34:37], off offset:512 sc1
	s_mov_b32 s1, 0x28000
	v_pk_mul_f32 v[16:17], v[16:17], s[2:3] op_sel_hi:[1,0]
	v_pk_mul_f32 v[36:37], v[88:89], s[2:3] op_sel_hi:[1,0]
	v_pk_mul_f32 v[34:35], v[86:87], s[2:3] op_sel_hi:[1,0]
	global_store_dwordx4 v[38:39], v[34:37], off offset:576 sc1
	v_lshl_add_u64 v[38:39], v[130:131], 0, s[4:5]
	s_mov_b64 s[4:5], 0x28000
	v_pk_mul_f32 v[36:37], v[64:65], s[2:3] op_sel_hi:[1,0]
	v_pk_mul_f32 v[34:35], v[62:63], s[2:3] op_sel_hi:[1,0]
	global_store_dwordx4 v[40:41], v[34:37], off sc1
	v_pk_mul_f32 v[14:15], v[14:15], s[2:3] op_sel_hi:[1,0]
	v_pk_mul_f32 v[4:5], v[4:5], s[2:3] op_sel_hi:[1,0]
	v_pk_mul_f32 v[36:37], v[52:53], s[2:3] op_sel_hi:[1,0]
	v_pk_mul_f32 v[34:35], v[50:51], s[2:3] op_sel_hi:[1,0]
	global_store_dwordx4 v[38:39], v[34:37], off offset:64 sc1
	v_pk_mul_f32 v[2:3], v[2:3], s[2:3] op_sel_hi:[1,0]
	global_store_dwordx4 v[130:131], v[122:125], off sc1
	v_pk_mul_f32 v[36:37], v[60:61], s[2:3] op_sel_hi:[1,0]
	v_pk_mul_f32 v[34:35], v[58:59], s[2:3] op_sel_hi:[1,0]
	global_store_dwordx4 v[38:39], v[34:37], off offset:512 sc1
	global_store_dwordx4 v[114:115], v[106:109], off sc1
	global_store_dwordx4 v[98:99], v[74:77], off sc1
	v_pk_mul_f32 v[36:37], v[56:57], s[2:3] op_sel_hi:[1,0]
	v_pk_mul_f32 v[34:35], v[54:55], s[2:3] op_sel_hi:[1,0]
	global_store_dwordx4 v[38:39], v[34:37], off offset:576 sc1
	global_store_dwordx4 v[66:67], v[42:45], off sc1
	s_cmpk_gt_u32 s0, 0xff
	v_lshl_add_u64 v[34:35], v[130:131], 0, s[4:5]
	v_add_co_u32_e32 v36, vcc, s1, v130
	global_store_dwordx4 v[34:35], v[18:21], off offset:64 sc1
	s_nop 0
	v_addc_co_u32_e32 v37, vcc, 0, v131, vcc
	v_pk_mul_f32 v[20:21], v[28:29], s[2:3] op_sel_hi:[1,0]
	v_pk_mul_f32 v[18:19], v[26:27], s[2:3] op_sel_hi:[1,0]
	global_store_dwordx4 v[34:35], v[18:21], off offset:512 sc1
	s_mov_b64 s[4:5], 0x2c000
	s_mov_b32 s1, 0x2c000
	v_pk_mul_f32 v[20:21], v[24:25], s[2:3] op_sel_hi:[1,0]
	v_pk_mul_f32 v[18:19], v[22:23], s[2:3] op_sel_hi:[1,0]
	global_store_dwordx4 v[34:35], v[18:21], off offset:576 sc1
	global_store_dwordx4 v[36:37], v[30:33], off sc1
	s_nop 0
	v_lshl_add_u64 v[18:19], v[130:131], 0, s[4:5]
	v_add_co_u32_e32 v20, vcc, s1, v130
	global_store_dwordx4 v[18:19], v[6:9], off offset:64 sc1
	s_nop 0
	v_addc_co_u32_e32 v21, vcc, 0, v131, vcc
	v_pk_mul_f32 v[8:9], v[12:13], s[2:3] op_sel_hi:[1,0]
	v_pk_mul_f32 v[6:7], v[10:11], s[2:3] op_sel_hi:[1,0]
	global_store_dwordx4 v[20:21], v[14:17], off sc1
	global_store_dwordx4 v[18:19], v[6:9], off offset:512 sc1
	global_store_dwordx4 v[18:19], v[2:5], off offset:576 sc1
	s_waitcnt vmcnt(0)
	s_cbranch_scc1 .LBB0_1445
	s_barrier

; #define PHASE(k) if constexpr (IN(k)) for (int rep_ = 0; rep_ < (((PROBE_MASK >> (k)) & 1u) ? 2 : 1); ++rep_)
; template <int LO, int HI, int l>
; __device__ __forceinline__ void layer_phases(Frame& F) {
;     ...
;     PHASE(pb + 2) {
;         launder(F);
;         if (F.vcu < F.G - 64) phase_conv(F, l, F.G - 64);
;         else { SchedF S{(const char*)WSP(unsigned char, WS_A8), (const char*)(WSP(unsigned char, WS_WF) + (size_t)l * NG * 256 * 1024), F.G, F.vcu};
;             EpiF32 E{WSP(float, WS_F), 256, (size_t)NINST * 256, S5_INV};
;             pg8::gemm_phase<EpiF32, SchedF, false, true>(F.lds, F.tid, pg8::Dims{KS2, 1024, 1024, nullptr}, S, E); }
;     }
.LBB0_1446:
	s_waitcnt vmcnt(0) lgkmcnt(0)
	s_barrier
	v_cmp_eq_u32_e64 s[98:99], 0, v0
	s_and_saveexec_b64 s[100:101], s[98:99]
	s_cbranch_execz .Lfd1_pw
	v_mov_b32_e32 v2, s33
	v_mov_b32_e32 v3, s40
	v_mov_b32_e32 v4, 1
	flat_atomic_add v[2:3], v4 offset:3840
	s_waitcnt vmcnt(0) lgkmcnt(0)

; #define GAS __attribute__((address_space(1)))
; #define PHASE(k) if constexpr (IN(k)) for (int rep_ = 0; rep_ < (((PROBE_MASK >> (k)) & 1u) ? 2 : 1); ++rep_)
; __device__ __forceinline__ void phase_carry(Frame& F, int l) {
;     const int gt = F.vcu * 512 + F.tid; if (gt >= NB * NG * 2 * SP) return;
;     const int p = gt & 63, d = (gt >> 6) & 1, g = (gt >> 7) & 31, b = gt >> 12;
;     const f32x2 lt = WSP(f32x2, WS_LT)[((l * NG + g) * 2 + d) * 64 + p];
;     const float* Fb = WSP(float, WS_F); unsigned char* a8 = WSP(unsigned char, WS_A8);
;     float hr = 0.f, hi = 0.f;
;     float frv[36], fiv[36];
; #pragma unroll
;     for (int step = 0; step < 36; ++step) {
;         int inst; if (step < 4) inst = 256 + b * 4 + (d == 0 ? step : 3 - step); else inst = b * 32 + (d == 0 ? step - 4 : 35 - step);
;         const size_t row = (size_t)g * NINST + inst;
;         frv[step] = *(const GAS float*)(Fb + row * 256 + d * 128 + p); fiv[step] = *(const GAS float*)(Fb + row * 256 + d * 128 + 64 + p); }
; #pragma unroll
;     for (int step = 0; step < 36; ++step) {
;         int inst; if (step < 4) inst = 256 + b * 4 + (d == 0 ? step : 3 - step); else inst = b * 32 + (d == 0 ? step - 4 : 35 - step);
; template <int LO, int HI, int l>
; __device__ __forceinline__ void layer_phases(Frame& F) {
;     ...
;     PHASE(pb + 3) { launder(F); phase_carry(F, l); }
.LBB0_1452:
	s_and_b32 s98, s95, 7
	s_lshl_b32 s98, s98, 5
	s_lshr_b32 s99, s95, 3
	s_add_i32 s98, s98, s99
	s_cmp_ge_u32 s98, 64
	s_cbranch_scc1 .Lfd1_done
	s_waitcnt vmcnt(0) lgkmcnt(0)
	v_cmp_eq_u32_e64 s[98:99], 0, v0
	s_and_saveexec_b64 s[100:101], s[98:99]
	s_cbranch_execz .Lfd1_w
	v_mov_b32_e32 v2, s33
	v_mov_b32_e32 v3, s40
	s_mov_b32 s98, 0
.Lfd1_poll:
	flat_load_dword v4, v[2:3] offset:3840 sc1
	s_waitcnt vmcnt(0) lgkmcnt(0)
	v_readfirstlane_b32 s99, v4
	s_add_u32 s98, s98, 1
	s_cmp_ge_u32 s99, 128
	s_cbranch_scc1 .Lfd1_go
	s_sleep 2
	s_cmp_lt_u32 s98, 0x4000
	s_cbranch_scc1 .Lfd1_poll

; #define GAS __attribute__((address_space(1)))
; __device__ __forceinline__ void phase_carry(Frame& F, int l) {
;     const int gt = F.vcu * 512 + F.tid; if (gt >= NB * NG * 2 * SP) return;
;     const int p = gt & 63, d = (gt >> 6) & 1, g = (gt >> 7) & 31, b = gt >> 12;
;     const f32x2 lt = WSP(f32x2, WS_LT)[((l * NG + g) * 2 + d) * 64 + p];
;     const float* Fb = WSP(float, WS_F); unsigned char* a8 = WSP(unsigned char, WS_A8);
;     float hr = 0.f, hi = 0.f;
;     float frv[36], fiv[36];
; #pragma unroll
;     for (int step = 0; step < 36; ++step) {
;         int inst; if (step < 4) inst = 256 + b * 4 + (d == 0 ? step : 3 - step); else inst = b * 32 + (d == 0 ? step - 4 : 35 - step);
;         const size_t row = (size_t)g * NINST + inst;
;         frv[step] = *(const GAS float*)(Fb + row * 256 + d * 128 + p); fiv[step] = *(const GAS float*)(Fb + row * 256 + d * 128 + 64 + p); }
; #pragma unroll
;     for (int step = 0; step < 36; ++step) {
;         int inst; if (step < 4) inst = 256 + b * 4 + (d == 0 ? step : 3 - step); else inst = b * 32 + (d == 0 ? step - 4 : 35 - step);
; __device__ __forceinline__ void launder(Frame& F) { F.ws = opaque_ptr(F.ws); F.out = opaque_ptr(F.out);
;     int t = F.tid; asm volatile("" : "+v"(t)); F.tid = t; F.lane = t & 63; F.wave = __builtin_amdgcn_readfirstlane(t >> 6);
;     int g = gridDim.x, bx = blockIdx.x; asm volatile("" : "+v"(g), "+v"(bx)); g = __builtin_amdgcn_readfirstlane(g); bx = __builtin_amdgcn_readfirstlane(bx);
;     F.G = g; F.vcu = (g % 8 == 0) ? (bx % 8) * (g / 8) + bx / 8 : bx; }
.Lfd1_w:
	s_or_b64 exec, exec, s[100:101]
	s_barrier
	v_writelane_b32 v254, s0, 0
	v_writelane_b32 v254, s1, 1
	v_writelane_b32 v254, s2, 2
	v_writelane_b32 v254, s3, 3
	v_writelane_b32 v254, s4, 4
	v_writelane_b32 v254, s5, 5
	v_writelane_b32 v254, s6, 6
	v_writelane_b32 v254, s7, 7
	v_writelane_b32 v254, s33, 8
	v_writelane_b32 v254, s40, 9
	v_mov_b32_e32 v1, s33
	v_mov_b32_e32 v2, s40
	s_nop 0
	s_nop 0
	v_readfirstlane_b32 s2, v1
	v_readfirstlane_b32 s3, v2
	v_mov_b32_e32 v1, s41
	v_mov_b32_e32 v2, s42
	s_nop 0
	v_readfirstlane_b32 s33, v1
	v_readfirstlane_b32 s40, v2
	v_mov_b32_e32 v1, s54
	v_mov_b32_e32 v2, s95
	s_nop 0
	v_readfirstlane_b32 s1, v1
	s_and_b32 s0, s1, 7
	s_cmp_eq_u32 s0, 0
	v_readfirstlane_b32 s0, v2
	s_cbranch_scc0 .Lfd1_1499
	s_ashr_i32 s4, s0, 31
	s_lshr_b32 s4, s4, 29
	s_add_i32 s4, s0, s4
	s_ashr_i32 s5, s4, 3
	s_and_b32 s4, s4, -8
	s_ashr_i32 s1, s1, 3
	s_sub_i32 s0, s0, s4
	s_mul_i32 s0, s0, s1
	s_add_i32 s0, s0, s5

; #define GAS __attribute__((address_space(1)))
; __device__ __forceinline__ void phase_carry(Frame& F, int l) {
;     const int gt = F.vcu * 512 + F.tid; if (gt >= NB * NG * 2 * SP) return;
;     const int p = gt & 63, d = (gt >> 6) & 1, g = (gt >> 7) & 31, b = gt >> 12;
;     const f32x2 lt = WSP(f32x2, WS_LT)[((l * NG + g) * 2 + d) * 64 + p];
;     const float* Fb = WSP(float, WS_F); unsigned char* a8 = WSP(unsigned char, WS_A8);
;     float hr = 0.f, hi = 0.f;
;     float frv[36], fiv[36];
; #pragma unroll
;     for (int step = 0; step < 36; ++step) {
;         int inst; if (step < 4) inst = 256 + b * 4 + (d == 0 ? step : 3 - step); else inst = b * 32 + (d == 0 ? step - 4 : 35 - step);
;         const size_t row = (size_t)g * NINST + inst;
;         frv[step] = *(const GAS float*)(Fb + row * 256 + d * 128 + p); fiv[step] = *(const GAS float*)(Fb + row * 256 + d * 128 + 64 + p); }
; #pragma unroll
;     for (int step = 0; step < 36; ++step) {
;         int inst; if (step < 4) inst = 256 + b * 4 + (d == 0 ? step : 3 - step); else inst = b * 32 + (d == 0 ? step - 4 : 35 - step);
;         const size_t row = (size_t)g * NINST + inst;
;         a8[row * KS2 + 1024 + d * 128 + p] = (unsigned char)(pk4_fp8(hr * S5_SH, 0.f, 0.f, 0.f) & 0xffu); a8[row * KS2 + 1024 + d * 128 + 64 + p] = (unsigned char)(pk4_fp8(hi * S5_SH, 0.f, 0.f, 0.f) & 0xffu);
;         const float nr = lt.x * hr - lt.y * hi + frv[step]; hi = lt.x * hi + lt.y * hr + fiv[step]; hr = nr; }
; }
.Lfd1_1501:
	s_or_b64 exec, exec, s[4:5]
	s_waitcnt vmcnt(0) lgkmcnt(0)
	v_readlane_b32 s0, v254, 0
	v_readlane_b32 s1, v254, 1
	v_readlane_b32 s2, v254, 2
	v_readlane_b32 s3, v254, 3
	v_readlane_b32 s4, v254, 4
	v_readlane_b32 s5, v254, 5
	v_readlane_b32 s6, v254, 6
	v_readlane_b32 s7, v254, 7
	v_readlane_b32 s33, v254, 8
	v_readlane_b32 s40, v254, 9

; #define PHASE(k) if constexpr (IN(k)) for (int rep_ = 0; rep_ < (((PROBE_MASK >> (k)) & 1u) ? 2 : 1); ++rep_)
; #define SEAM(k) do { if constexpr (IN(k) && IN((k) + 1)) grid_seam(F); } while (0)
; __device__ __forceinline__ void launder(Frame& F) { F.ws = opaque_ptr(F.ws); F.out = opaque_ptr(F.out);
;     int t = F.tid; asm volatile("" : "+v"(t)); F.tid = t; F.lane = t & 63; F.wave = __builtin_amdgcn_readfirstlane(t >> 6);
;     int g = gridDim.x, bx = blockIdx.x; asm volatile("" : "+v"(g), "+v"(bx)); g = __builtin_amdgcn_readfirstlane(g); bx = __builtin_amdgcn_readfirstlane(bx);
;     F.G = g; F.vcu = (g % 8 == 0) ? (bx % 8) * (g / 8) + bx / 8 : bx; }
; template <int LO, int HI, int l>
; __device__ __forceinline__ void layer_phases(Frame& F) {
;     ...
;     PHASE(pb + 3) { launder(F); phase_carry(F, l); }
;     SEAM(pb + 3);
.LBB0_1497:
	s_or_b64 exec, exec, s[2:3]
	v_mov_b32_e32 v1, s33
	v_mov_b32_e32 v2, s40
	s_waitcnt lgkmcnt(0)
	s_barrier
	s_nop 0
	v_readfirstlane_b32 s2, v1
	v_readfirstlane_b32 s3, v2
	v_mov_b32_e32 v1, s41
	v_mov_b32_e32 v2, s42
	s_nop 0
	v_readfirstlane_b32 s33, v1
	v_readfirstlane_b32 s40, v2
	s_branch .Lfd1_end
	v_mov_b32_e32 v1, s54
	v_mov_b32_e32 v2, s95
	s_nop 0
	v_readfirstlane_b32 s1, v1
	s_and_b32 s0, s1, 7
	s_cmp_eq_u32 s0, 0
	v_readfirstlane_b32 s0, v2
	s_cbranch_scc0 .LBB0_1499
	s_ashr_i32 s4, s0, 31
	s_lshr_b32 s4, s4, 29
	s_add_i32 s4, s0, s4
	s_ashr_i32 s5, s4, 3
	s_and_b32 s4, s4, -8
	s_ashr_i32 s1, s1, 3
	s_sub_i32 s0, s0, s4
	s_mul_i32 s0, s0, s1
	s_add_i32 s0, s0, s5

; #define PHASE(k) if constexpr (IN(k)) for (int rep_ = 0; rep_ < (((PROBE_MASK >> (k)) & 1u) ? 2 : 1); ++rep_)
; __device__ __forceinline__ void launder(Frame& F) { F.ws = opaque_ptr(F.ws); F.out = opaque_ptr(F.out);
;     int t = F.tid; asm volatile("" : "+v"(t)); F.tid = t; F.lane = t & 63; F.wave = __builtin_amdgcn_readfirstlane(t >> 6);
;     int g = gridDim.x, bx = blockIdx.x; asm volatile("" : "+v"(g), "+v"(bx)); g = __builtin_amdgcn_readfirstlane(g); bx = __builtin_amdgcn_readfirstlane(bx);
;     F.G = g; F.vcu = (g % 8 == 0) ? (bx % 8) * (g / 8) + bx / 8 : bx; }
; template <int LO, int HI, int l>
; __device__ __forceinline__ void layer_phases(Frame& F) {
;     ...
;     PHASE(pb + 4) {
;         launder(F);
;         SchedS2 S{(const char*)WSP(unsigned char, WS_A8), (const char*)(WSP(unsigned char, WS_W2) + (size_t)l * NG * 1024 * KS2), F.G, F.vcu, l};
;         EpiS2 E{WSP(bf16, WS_U2), F.in[I_SSMD] + (size_t)l * DSSM, WSP(bf16, WS_Z)};
;         pg8::gemm_phase<EpiS2, SchedS2, true, true>(F.lds, F.tid, pg8::Dims{KS2, KS2, KS2, nullptr}, S, E);
.Lfd1_end:
	v_mov_b32_e32 v1, s2
	v_mov_b32_e32 v2, s3
	s_waitcnt lgkmcnt(0)
	s_barrier
	s_nop 0
	v_readfirstlane_b32 s42, v1
	v_readfirstlane_b32 s43, v2
	v_mov_b32_e32 v1, s33
	v_mov_b32_e32 v2, s40
	s_nop 0
	v_readfirstlane_b32 s55, v1
	v_readfirstlane_b32 s56, v2
	v_mov_b32_e32 v1, s54
	v_mov_b32_e32 v2, s95
	v_readfirstlane_b32 s33, v0
	v_readfirstlane_b32 s57, v1
	s_and_b32 s0, s57, 7
	s_cmp_eq_u32 s0, 0
	v_readfirstlane_b32 s58, v2
	s_cbranch_scc0 .LBB0_1548
	s_ashr_i32 s1, s58, 31
	s_lshr_b32 s1, s1, 29
	s_add_i32 s1, s58, s1
	s_ashr_i32 s2, s1, 3
	s_and_b32 s1, s1, -8
	s_ashr_i32 s0, s57, 3
	s_sub_i32 s1, s58, s1
	s_mul_i32 s0, s1, s0
	s_add_i32 s58, s0, s2
